# v40: v38 + LDS-DMA staging rebalanced 4/4/4/4 in six more GEMM K-loops (in-proj x2, MLA q-up, Wo, dense down, MoE down)
# speedup vs baseline: 1.0081x; 1.0002x over previous
.LBB0_689:
	s_add_u32 s26, s21, s10
	s_addc_u32 s27, s22, s11
	s_add_u32 s12, s26, 0x15000100
	s_addc_u32 s13, s27, 0
	s_add_u32 s14, s23, s10
	s_addc_u32 s15, s24, s11
	s_add_i32 s28, 0, 0x10000
	s_cmpk_eq_i32 s10, 0x300
	s_cselect_b32 s13, s9, s13
	s_cselect_b32 s12, s8, s12
	v_add_u32_e32 v0, s28, v38
	s_cselect_b32 s15, s7, s15
	s_cselect_b32 s14, s6, s14
	s_add_i32 s29, 0, 0x14000
	ds_read_b128 v[138:141], v0
	ds_read_b128 v[142:145], v0 offset:1024
	ds_read_b128 v[146:149], v0 offset:2048
	ds_read_b128 v[150:153], v0 offset:3072
	v_add_u32_e32 v0, s29, v38
	ds_read_b128 v[154:157], v0
	ds_read_b128 v[158:161], v0 offset:1024
	ds_read_b128 v[162:165], v0 offset:2048
	ds_read_b128 v[166:169], v0 offset:3072
	v_mov_b32_e32 v0, v34
	ds_read_b128 v[170:173], v39
	ds_read_b128 v[174:177], v39 offset:1024
	ds_read_b128 v[178:181], v39 offset:2048
	ds_read_b128 v[182:185], v39 offset:3072
	ds_read_b128 v[186:189], v39 offset:4096
	ds_read_b128 v[190:193], v39 offset:5120
	ds_read_b128 v[194:197], v39 offset:6144
	ds_read_b128 v[198:201], v39 offset:7168
	s_add_i32 m0, s85, 0xc000
	v_lshl_add_u64 v[40:41], s[26:27], 0, v[0:1]
	v_lshl_add_u64 v[40:41], v[40:41], 0, s[64:65]
	v_mov_b32_e32 v0, v36
	global_load_lds_dwordx4 v[40:41], off
	s_add_i32 m0, s85, 0xe000
	v_lshl_add_u64 v[40:41], s[26:27], 0, v[0:1]
	v_lshl_add_u64 v[40:41], v[40:41], 0, s[64:65]
	global_load_lds_dwordx4 v[40:41], off
	s_waitcnt vmcnt(8)
	s_waitcnt lgkmcnt(0)
	s_barrier
	s_setprio 1
	s_waitcnt lgkmcnt(0)
	v_mfma_i32_16x16x64_i8 v[134:137], v[138:141], v[170:173], v[134:137]
	v_mfma_i32_16x16x64_i8 v[130:133], v[146:149], v[170:173], v[130:133]
	v_mfma_i32_16x16x64_i8 v[126:129], v[138:141], v[178:181], v[126:129]
	v_mfma_i32_16x16x64_i8 v[122:125], v[146:149], v[178:181], v[122:125]
	v_mfma_i32_16x16x64_i8 v[118:121], v[138:141], v[186:189], v[118:121]
	v_mfma_i32_16x16x64_i8 v[114:117], v[146:149], v[186:189], v[114:117]
	v_mfma_i32_16x16x64_i8 v[110:113], v[138:141], v[194:197], v[110:113]
	v_mfma_i32_16x16x64_i8 v[106:109], v[146:149], v[194:197], v[106:109]
	v_mfma_i32_16x16x64_i8 v[134:137], v[142:145], v[174:177], v[134:137]
	v_mfma_i32_16x16x64_i8 v[130:133], v[150:153], v[174:177], v[130:133]
	v_mfma_i32_16x16x64_i8 v[126:129], v[142:145], v[182:185], v[126:129]
	v_mfma_i32_16x16x64_i8 v[122:125], v[150:153], v[182:185], v[122:125]
	v_mfma_i32_16x16x64_i8 v[118:121], v[142:145], v[190:193], v[118:121]
	v_mfma_i32_16x16x64_i8 v[114:117], v[150:153], v[190:193], v[114:117]
	v_mfma_i32_16x16x64_i8 v[110:113], v[142:145], v[198:201], v[110:113]
	v_mfma_i32_16x16x64_i8 v[106:109], v[150:153], v[198:201], v[106:109]
	s_setprio 0
	s_setprio 1
	v_mfma_i32_16x16x64_i8 v[78:81], v[154:157], v[170:173], v[78:81]
	v_mfma_i32_16x16x64_i8 v[74:77], v[162:165], v[170:173], v[74:77]
	v_mfma_i32_16x16x64_i8 v[62:65], v[154:157], v[178:181], v[62:65]
	v_mfma_i32_16x16x64_i8 v[58:61], v[162:165], v[178:181], v[58:61]
	v_mfma_i32_16x16x64_i8 v[54:57], v[154:157], v[186:189], v[54:57]
	v_mfma_i32_16x16x64_i8 v[50:53], v[162:165], v[186:189], v[50:53]
	v_mfma_i32_16x16x64_i8 v[46:49], v[154:157], v[194:197], v[46:49]
	v_mfma_i32_16x16x64_i8 v[40:43], v[162:165], v[194:197], v[42:45]
	v_mfma_i32_16x16x64_i8 v[78:81], v[158:161], v[174:177], v[78:81]
	v_mfma_i32_16x16x64_i8 v[74:77], v[166:169], v[174:177], v[74:77]
	v_mfma_i32_16x16x64_i8 v[62:65], v[158:161], v[182:185], v[62:65]
	v_mfma_i32_16x16x64_i8 v[58:61], v[166:169], v[182:185], v[58:61]
	v_mfma_i32_16x16x64_i8 v[54:57], v[158:161], v[190:193], v[54:57]
	v_mfma_i32_16x16x64_i8 v[50:53], v[166:169], v[190:193], v[50:53]
	v_mfma_i32_16x16x64_i8 v[46:49], v[158:161], v[198:201], v[46:49]
	v_mfma_i32_16x16x64_i8 v[40:43], v[166:169], v[198:201], v[40:43]
	s_setprio 0
	s_barrier
	v_mov_b32_e32 v0, v35
	s_add_i32 s26, s28, s33
	ds_read_b128 v[170:173], v39 offset:16384
	ds_read_b128 v[174:177], v39 offset:17408
	ds_read_b128 v[178:181], v39 offset:18432
	ds_read_b128 v[182:185], v39 offset:19456
	ds_read_b128 v[186:189], v39 offset:20480
	ds_read_b128 v[190:193], v39 offset:21504
	ds_read_b128 v[194:197], v39 offset:22528
	ds_read_b128 v[198:201], v39 offset:23552
	s_mov_b32 m0, s26
	s_nop 0
	global_load_lds_dwordx4 v0, s[14:15]
	v_mov_b32_e32 v0, v37
	s_add_i32 m0, s26, 0x2000
	s_add_u32 s26, s14, 0x20000
	global_load_lds_dwordx4 v0, s[14:15]
	s_addc_u32 s27, s15, 0
	v_mov_b32_e32 v0, v35
	s_add_i32 s28, s29, s33
	s_mov_b32 m0, s28
	s_nop 0
	global_load_lds_dwordx4 v0, s[26:27]
	v_mov_b32_e32 v0, v37
	s_add_i32 m0, s28, 0x2000
	s_nop 0
	global_load_lds_dwordx4 v0, s[26:27]
	s_waitcnt vmcnt(6)
	s_waitcnt lgkmcnt(0)
	s_barrier
	s_setprio 1
	s_waitcnt lgkmcnt(0)
	v_mfma_i32_16x16x64_i8 v[102:105], v[138:141], v[170:173], v[102:105]
	v_mfma_i32_16x16x64_i8 v[98:101], v[146:149], v[170:173], v[98:101]
	v_mfma_i32_16x16x64_i8 v[94:97], v[138:141], v[178:181], v[94:97]
	v_mfma_i32_16x16x64_i8 v[90:93], v[146:149], v[178:181], v[90:93]
	v_mfma_i32_16x16x64_i8 v[86:89], v[138:141], v[186:189], v[86:89]
	v_mfma_i32_16x16x64_i8 v[82:85], v[146:149], v[186:189], v[82:85]
	v_mfma_i32_16x16x64_i8 v[70:73], v[138:141], v[194:197], v[70:73]
	v_mfma_i32_16x16x64_i8 v[66:69], v[146:149], v[194:197], v[66:69]
	v_mfma_i32_16x16x64_i8 v[102:105], v[142:145], v[174:177], v[102:105]
	v_mfma_i32_16x16x64_i8 v[98:101], v[150:153], v[174:177], v[98:101]
	v_mfma_i32_16x16x64_i8 v[94:97], v[142:145], v[182:185], v[94:97]
	v_mfma_i32_16x16x64_i8 v[90:93], v[150:153], v[182:185], v[90:93]
	v_mfma_i32_16x16x64_i8 v[86:89], v[142:145], v[190:193], v[86:89]
	v_mfma_i32_16x16x64_i8 v[82:85], v[150:153], v[190:193], v[82:85]
	v_mfma_i32_16x16x64_i8 v[70:73], v[142:145], v[198:201], v[70:73]
	v_mfma_i32_16x16x64_i8 v[66:69], v[150:153], v[198:201], v[66:69]
	s_setprio 0
	s_setprio 1
	v_mfma_i32_16x16x64_i8 v[30:33], v[154:157], v[170:173], v[30:33]
	v_mfma_i32_16x16x64_i8 v[26:29], v[162:165], v[170:173], v[26:29]
	v_mfma_i32_16x16x64_i8 v[22:25], v[154:157], v[178:181], v[22:25]
	v_mfma_i32_16x16x64_i8 v[18:21], v[162:165], v[178:181], v[18:21]
	v_mfma_i32_16x16x64_i8 v[14:17], v[154:157], v[186:189], v[14:17]
	v_mfma_i32_16x16x64_i8 v[10:13], v[162:165], v[186:189], v[10:13]
	v_mfma_i32_16x16x64_i8 v[6:9], v[154:157], v[194:197], v[6:9]
	v_mfma_i32_16x16x64_i8 v[2:5], v[162:165], v[194:197], v[2:5]
	v_mfma_i32_16x16x64_i8 v[30:33], v[158:161], v[174:177], v[30:33]
	v_mfma_i32_16x16x64_i8 v[26:29], v[166:169], v[174:177], v[26:29]
	v_mfma_i32_16x16x64_i8 v[22:25], v[158:161], v[182:185], v[22:25]
	v_mfma_i32_16x16x64_i8 v[18:21], v[166:169], v[182:185], v[18:21]
	v_mfma_i32_16x16x64_i8 v[14:17], v[158:161], v[190:193], v[14:17]
	v_mfma_i32_16x16x64_i8 v[10:13], v[166:169], v[190:193], v[10:13]
	v_mfma_i32_16x16x64_i8 v[6:9], v[158:161], v[198:201], v[6:9]
	v_mfma_i32_16x16x64_i8 v[2:5], v[166:169], v[198:201], v[2:5]
	s_setprio 0
	s_barrier
	s_add_i32 s28, 0, 0x18000
	v_add_u32_e32 v0, s28, v38
	s_add_i32 s29, 0, 0x1c000
	ds_read_b128 v[138:141], v0
	ds_read_b128 v[142:145], v0 offset:1024
	ds_read_b128 v[146:149], v0 offset:2048
	ds_read_b128 v[150:153], v0 offset:3072
	v_add_u32_e32 v0, s29, v38
	ds_read_b128 v[154:157], v0
	ds_read_b128 v[158:161], v0 offset:1024
	ds_read_b128 v[162:165], v0 offset:2048
	ds_read_b128 v[166:169], v0 offset:3072
	s_add_u32 s26, s12, 0x20000
	ds_read_b128 v[170:173], v39 offset:32768
	ds_read_b128 v[174:177], v39 offset:33792
	ds_read_b128 v[178:181], v39 offset:34816
	ds_read_b128 v[182:185], v39 offset:35840
	ds_read_b128 v[186:189], v39 offset:36864
	ds_read_b128 v[190:193], v39 offset:37888
	ds_read_b128 v[194:197], v39 offset:38912
	ds_read_b128 v[198:201], v39 offset:39936
	s_addc_u32 s27, s13, 0
	v_mov_b32_e32 v0, v34
	s_mov_b32 m0, s85
	s_nop 0
	global_load_lds_dwordx4 v0, s[12:13]
	v_mov_b32_e32 v0, v36
	s_mov_b32 m0, s3
	s_nop 0
	global_load_lds_dwordx4 v0, s[12:13]
	v_mov_b32_e32 v0, v34
	s_mov_b32 m0, s17
	s_nop 0
	global_load_lds_dwordx4 v0, s[26:27]
	v_mov_b32_e32 v0, v36
	s_mov_b32 m0, s18
	s_nop 0
	global_load_lds_dwordx4 v0, s[26:27]
	s_waitcnt vmcnt(8)
	s_waitcnt lgkmcnt(0)
	s_barrier
	s_setprio 1
	s_waitcnt lgkmcnt(0)
	v_mfma_i32_16x16x64_i8 v[134:137], v[138:141], v[170:173], v[134:137]
	v_mfma_i32_16x16x64_i8 v[130:133], v[146:149], v[170:173], v[130:133]
	v_mfma_i32_16x16x64_i8 v[126:129], v[138:141], v[178:181], v[126:129]
	v_mfma_i32_16x16x64_i8 v[122:125], v[146:149], v[178:181], v[122:125]
	v_mfma_i32_16x16x64_i8 v[118:121], v[138:141], v[186:189], v[118:121]
	v_mfma_i32_16x16x64_i8 v[114:117], v[146:149], v[186:189], v[114:117]
	v_mfma_i32_16x16x64_i8 v[110:113], v[138:141], v[194:197], v[110:113]
	v_mfma_i32_16x16x64_i8 v[106:109], v[146:149], v[194:197], v[106:109]
	v_mfma_i32_16x16x64_i8 v[134:137], v[142:145], v[174:177], v[134:137]
	v_mfma_i32_16x16x64_i8 v[130:133], v[150:153], v[174:177], v[130:133]
	v_mfma_i32_16x16x64_i8 v[126:129], v[142:145], v[182:185], v[126:129]
	v_mfma_i32_16x16x64_i8 v[122:125], v[150:153], v[182:185], v[122:125]
	v_mfma_i32_16x16x64_i8 v[118:121], v[142:145], v[190:193], v[118:121]
	v_mfma_i32_16x16x64_i8 v[114:117], v[150:153], v[190:193], v[114:117]
	v_mfma_i32_16x16x64_i8 v[110:113], v[142:145], v[198:201], v[110:113]
	v_mfma_i32_16x16x64_i8 v[106:109], v[150:153], v[198:201], v[106:109]
	s_setprio 0
	s_setprio 1
	v_mfma_i32_16x16x64_i8 v[78:81], v[154:157], v[170:173], v[78:81]
	v_mfma_i32_16x16x64_i8 v[74:77], v[162:165], v[170:173], v[74:77]
	v_mfma_i32_16x16x64_i8 v[62:65], v[154:157], v[178:181], v[62:65]
	v_mfma_i32_16x16x64_i8 v[58:61], v[162:165], v[178:181], v[58:61]
	v_mfma_i32_16x16x64_i8 v[54:57], v[154:157], v[186:189], v[54:57]
	v_mfma_i32_16x16x64_i8 v[50:53], v[162:165], v[186:189], v[50:53]
	v_mfma_i32_16x16x64_i8 v[44:47], v[154:157], v[194:197], v[46:49]
	v_mfma_i32_16x16x64_i8 v[40:43], v[162:165], v[194:197], v[40:43]
	v_mfma_i32_16x16x64_i8 v[78:81], v[158:161], v[174:177], v[78:81]
	v_mfma_i32_16x16x64_i8 v[74:77], v[166:169], v[174:177], v[74:77]
	v_mfma_i32_16x16x64_i8 v[62:65], v[158:161], v[182:185], v[62:65]
	v_mfma_i32_16x16x64_i8 v[58:61], v[166:169], v[182:185], v[58:61]
	v_mfma_i32_16x16x64_i8 v[54:57], v[158:161], v[190:193], v[54:57]
	v_mfma_i32_16x16x64_i8 v[50:53], v[166:169], v[190:193], v[50:53]
	v_mfma_i32_16x16x64_i8 v[46:49], v[158:161], v[198:201], v[44:47]
	v_mfma_i32_16x16x64_i8 v[42:45], v[166:169], v[198:201], v[40:43]
	s_setprio 0
	s_barrier
	v_mov_b32_e32 v0, v35
	ds_read_b128 v[170:173], v39 offset:49152
	ds_read_b128 v[174:177], v39 offset:50176
	ds_read_b128 v[178:181], v39 offset:51200
	ds_read_b128 v[182:185], v39 offset:52224
	ds_read_b128 v[186:189], v39 offset:53248
	ds_read_b128 v[190:193], v39 offset:54272
	ds_read_b128 v[194:197], v39 offset:55296
	ds_read_b128 v[198:201], v39 offset:56320
	s_add_i32 s26, s28, s33
	v_lshl_add_u64 v[40:41], s[14:15], 0, v[0:1]
	v_lshl_add_u64 v[40:41], v[40:41], 0, s[90:91]
	s_mov_b32 m0, s26
	v_mov_b32_e32 v0, v37
	global_load_lds_dwordx4 v[40:41], off
	s_add_i32 m0, s26, 0x2000
	s_nop 0
	v_lshl_add_u64 v[40:41], s[14:15], 0, v[0:1]
	s_add_u32 s14, s14, 0x20080
	v_lshl_add_u64 v[40:41], v[40:41], 0, s[90:91]
	s_addc_u32 s15, s15, 0
	v_mov_b32_e32 v0, v35
	s_add_i32 s26, s29, s33
	global_load_lds_dwordx4 v[40:41], off
	s_mov_b32 m0, s26
	s_nop 0
	global_load_lds_dwordx4 v0, s[14:15]
	v_mov_b32_e32 v0, v37
	s_add_i32 m0, s26, 0x2000
	s_nop 0
	global_load_lds_dwordx4 v0, s[14:15]
	s_waitcnt vmcnt(6)
	s_waitcnt lgkmcnt(0)
	s_barrier
	s_setprio 1
	s_waitcnt lgkmcnt(0)
	v_mfma_i32_16x16x64_i8 v[102:105], v[138:141], v[170:173], v[102:105]
	v_mfma_i32_16x16x64_i8 v[98:101], v[146:149], v[170:173], v[98:101]
	v_mfma_i32_16x16x64_i8 v[94:97], v[138:141], v[178:181], v[94:97]
	v_mfma_i32_16x16x64_i8 v[90:93], v[146:149], v[178:181], v[90:93]
	v_mfma_i32_16x16x64_i8 v[86:89], v[138:141], v[186:189], v[86:89]
	v_mfma_i32_16x16x64_i8 v[82:85], v[146:149], v[186:189], v[82:85]
	v_mfma_i32_16x16x64_i8 v[70:73], v[138:141], v[194:197], v[70:73]
	v_mfma_i32_16x16x64_i8 v[66:69], v[146:149], v[194:197], v[66:69]
	v_mfma_i32_16x16x64_i8 v[102:105], v[142:145], v[174:177], v[102:105]
	v_mfma_i32_16x16x64_i8 v[98:101], v[150:153], v[174:177], v[98:101]
	v_mfma_i32_16x16x64_i8 v[94:97], v[142:145], v[182:185], v[94:97]
	v_mfma_i32_16x16x64_i8 v[90:93], v[150:153], v[182:185], v[90:93]
	v_mfma_i32_16x16x64_i8 v[86:89], v[142:145], v[190:193], v[86:89]
	v_mfma_i32_16x16x64_i8 v[82:85], v[150:153], v[190:193], v[82:85]
	v_mfma_i32_16x16x64_i8 v[70:73], v[142:145], v[198:201], v[70:73]
	v_mfma_i32_16x16x64_i8 v[66:69], v[150:153], v[198:201], v[66:69]
	s_setprio 0
	s_setprio 1
	v_mfma_i32_16x16x64_i8 v[30:33], v[154:157], v[170:173], v[30:33]
	v_mfma_i32_16x16x64_i8 v[26:29], v[162:165], v[170:173], v[26:29]
	v_mfma_i32_16x16x64_i8 v[22:25], v[154:157], v[178:181], v[22:25]
	v_mfma_i32_16x16x64_i8 v[18:21], v[162:165], v[178:181], v[18:21]
	v_mfma_i32_16x16x64_i8 v[14:17], v[154:157], v[186:189], v[14:17]
	v_mfma_i32_16x16x64_i8 v[10:13], v[162:165], v[186:189], v[10:13]
	v_mfma_i32_16x16x64_i8 v[6:9], v[154:157], v[194:197], v[6:9]
	v_mfma_i32_16x16x64_i8 v[2:5], v[162:165], v[194:197], v[2:5]
	v_mfma_i32_16x16x64_i8 v[30:33], v[158:161], v[174:177], v[30:33]
	v_mfma_i32_16x16x64_i8 v[26:29], v[166:169], v[174:177], v[26:29]
	v_mfma_i32_16x16x64_i8 v[22:25], v[158:161], v[182:185], v[22:25]
	v_mfma_i32_16x16x64_i8 v[18:21], v[166:169], v[182:185], v[18:21]
	v_mfma_i32_16x16x64_i8 v[14:17], v[158:161], v[190:193], v[14:17]
	v_mfma_i32_16x16x64_i8 v[10:13], v[166:169], v[190:193], v[10:13]
	v_mfma_i32_16x16x64_i8 v[6:9], v[158:161], v[198:201], v[6:9]
	v_mfma_i32_16x16x64_i8 v[2:5], v[166:169], v[198:201], v[2:5]
	s_setprio 0
	s_barrier
	v_mov_b32_e32 v0, v34
	s_mov_b32 m0, s19
	v_lshl_add_u64 v[40:41], s[12:13], 0, v[0:1]
	v_lshl_add_u64 v[40:41], v[40:41], 0, s[90:91]
	v_mov_b32_e32 v0, v36
	global_load_lds_dwordx4 v[40:41], off
	s_mov_b32 m0, s20
	v_lshl_add_u64 v[40:41], s[12:13], 0, v[0:1]
	v_lshl_add_u64 v[40:41], v[40:41], 0, s[90:91]
	global_load_lds_dwordx4 v[40:41], off
	s_add_i32 s25, s25, 2
	s_add_u32 s10, s10, 0x100
	s_addc_u32 s11, s11, 0
	s_cmp_gt_u32 s25, 5
	s_cbranch_scc0 .LBB0_689
	v_readlane_b32 s6, v254, 19
	v_readlane_b32 s7, v254, 20
	s_and_b64 vcc, exec, s[6:7]
	s_cbranch_vccz .LBB0_692
	s_barrier

.LBB0_775:
	s_add_u32 s28, s8, 0xfffe0080
	s_addc_u32 s29, s9, -1
	s_add_i32 s43, 0, 0x10000
	s_cmp_eq_u32 s68, 4
	s_cselect_b32 s29, s3, s29
	s_cselect_b32 s28, s2, s28
	v_add_u32_e32 v0, s43, v198
	s_cselect_b32 s31, s64, s67
	s_cselect_b32 s30, s65, s66
	s_add_i32 s44, 0, 0x14000
	ds_read_b128 v[114:117], v0
	ds_read_b128 v[118:121], v0 offset:1024
	ds_read_b128 v[138:141], v0 offset:2048
	ds_read_b128 v[142:145], v0 offset:3072
	v_add_u32_e32 v0, s44, v198
	ds_read_b128 v[146:149], v0
	ds_read_b128 v[150:153], v0 offset:1024
	ds_read_b128 v[154:157], v0 offset:2048
	ds_read_b128 v[158:161], v0 offset:3072
	v_mov_b32_e32 v0, v194
	s_add_i32 s45, s85, 0xc000
	ds_read_b128 v[162:165], v199
	ds_read_b128 v[166:169], v199 offset:1024
	ds_read_b128 v[170:173], v199 offset:2048
	ds_read_b128 v[174:177], v199 offset:3072
	ds_read_b128 v[178:181], v199 offset:4096
	ds_read_b128 v[182:185], v199 offset:5120
	ds_read_b128 v[186:189], v199 offset:6144
	ds_read_b128 v[190:193], v199 offset:7168
	s_mov_b32 m0, s45
	s_add_i32 s46, s85, 0xe000
	global_load_lds_dwordx4 v0, s[8:9]
	v_mov_b32_e32 v0, v196
	s_mov_b32 m0, s46
	s_nop 0
	global_load_lds_dwordx4 v0, s[8:9]
	s_waitcnt vmcnt(8)
	s_waitcnt lgkmcnt(0)
	s_barrier
	s_setprio 1
	s_waitcnt lgkmcnt(0)
	v_mfma_i32_16x16x64_i8 v[134:137], v[114:117], v[162:165], v[134:137]
	v_mfma_i32_16x16x64_i8 v[130:133], v[138:141], v[162:165], v[130:133]
	v_mfma_i32_16x16x64_i8 v[126:129], v[114:117], v[170:173], v[126:129]
	v_mfma_i32_16x16x64_i8 v[122:125], v[138:141], v[170:173], v[122:125]
	v_mfma_i32_16x16x64_i8 v[110:113], v[114:117], v[178:181], v[110:113]
	v_mfma_i32_16x16x64_i8 v[106:109], v[138:141], v[178:181], v[106:109]
	v_mfma_i32_16x16x64_i8 v[102:105], v[114:117], v[186:189], v[102:105]
	v_mfma_i32_16x16x64_i8 v[98:101], v[138:141], v[186:189], v[98:101]
	v_mfma_i32_16x16x64_i8 v[134:137], v[118:121], v[166:169], v[134:137]
	v_mfma_i32_16x16x64_i8 v[130:133], v[142:145], v[166:169], v[130:133]
	v_mfma_i32_16x16x64_i8 v[126:129], v[118:121], v[174:177], v[126:129]
	v_mfma_i32_16x16x64_i8 v[122:125], v[142:145], v[174:177], v[122:125]
	v_mfma_i32_16x16x64_i8 v[110:113], v[118:121], v[182:185], v[110:113]
	v_mfma_i32_16x16x64_i8 v[106:109], v[142:145], v[182:185], v[106:109]
	v_mfma_i32_16x16x64_i8 v[102:105], v[118:121], v[190:193], v[102:105]
	v_mfma_i32_16x16x64_i8 v[98:101], v[142:145], v[190:193], v[98:101]
	s_setprio 0
	s_setprio 1
	v_mfma_i32_16x16x64_i8 v[62:65], v[146:149], v[162:165], v[62:65]
	v_mfma_i32_16x16x64_i8 v[58:61], v[154:157], v[162:165], v[58:61]
	v_mfma_i32_16x16x64_i8 v[54:57], v[146:149], v[170:173], v[54:57]
	v_mfma_i32_16x16x64_i8 v[50:53], v[154:157], v[170:173], v[50:53]
	v_mfma_i32_16x16x64_i8 v[46:49], v[146:149], v[178:181], v[46:49]
	v_mfma_i32_16x16x64_i8 v[42:45], v[154:157], v[178:181], v[42:45]
	v_mfma_i32_16x16x64_i8 v[38:41], v[146:149], v[186:189], v[38:41]
	v_mfma_i32_16x16x64_i8 v[34:37], v[154:157], v[186:189], v[34:37]
	v_mfma_i32_16x16x64_i8 v[62:65], v[150:153], v[166:169], v[62:65]
	v_mfma_i32_16x16x64_i8 v[58:61], v[158:161], v[166:169], v[58:61]
	v_mfma_i32_16x16x64_i8 v[54:57], v[150:153], v[174:177], v[54:57]
	v_mfma_i32_16x16x64_i8 v[50:53], v[158:161], v[174:177], v[50:53]
	v_mfma_i32_16x16x64_i8 v[46:49], v[150:153], v[182:185], v[46:49]
	v_mfma_i32_16x16x64_i8 v[42:45], v[158:161], v[182:185], v[42:45]
	v_mfma_i32_16x16x64_i8 v[38:41], v[150:153], v[190:193], v[38:41]
	v_mfma_i32_16x16x64_i8 v[34:37], v[158:161], v[190:193], v[34:37]
	s_setprio 0
	s_barrier
	v_mov_b32_e32 v0, v195
	s_add_i32 s47, s43, s33
	ds_read_b128 v[162:165], v199 offset:16384
	ds_read_b128 v[166:169], v199 offset:17408
	ds_read_b128 v[170:173], v199 offset:18432
	ds_read_b128 v[174:177], v199 offset:19456
	ds_read_b128 v[178:181], v199 offset:20480
	ds_read_b128 v[182:185], v199 offset:21504
	ds_read_b128 v[186:189], v199 offset:22528
	ds_read_b128 v[190:193], v199 offset:23552
	s_mov_b32 m0, s47
	s_add_i32 s48, s47, 0x2000
	global_load_lds_dwordx4 v0, s[30:31]
	v_mov_b32_e32 v0, v197
	s_mov_b32 m0, s48
	s_add_u32 s52, s30, 0x20000
	global_load_lds_dwordx4 v0, s[30:31]
	s_addc_u32 s53, s31, 0
	v_mov_b32_e32 v0, v195
	s_add_i32 s49, s44, s33
	s_mov_b32 m0, s49
	s_add_i32 s50, s49, 0x2000
	global_load_lds_dwordx4 v0, s[52:53]
	v_mov_b32_e32 v0, v197
	s_mov_b32 m0, s50
	s_nop 0
	global_load_lds_dwordx4 v0, s[52:53]
	s_waitcnt vmcnt(6)
	s_waitcnt lgkmcnt(0)
	s_barrier
	s_setprio 1
	s_waitcnt lgkmcnt(0)
	v_mfma_i32_16x16x64_i8 v[94:97], v[114:117], v[162:165], v[94:97]
	v_mfma_i32_16x16x64_i8 v[90:93], v[138:141], v[162:165], v[90:93]
	v_mfma_i32_16x16x64_i8 v[86:89], v[114:117], v[170:173], v[86:89]
	v_mfma_i32_16x16x64_i8 v[82:85], v[138:141], v[170:173], v[82:85]
	v_mfma_i32_16x16x64_i8 v[78:81], v[114:117], v[178:181], v[78:81]
	v_mfma_i32_16x16x64_i8 v[74:77], v[138:141], v[178:181], v[74:77]
	v_mfma_i32_16x16x64_i8 v[70:73], v[114:117], v[186:189], v[70:73]
	v_mfma_i32_16x16x64_i8 v[66:69], v[138:141], v[186:189], v[66:69]
	v_mfma_i32_16x16x64_i8 v[94:97], v[118:121], v[166:169], v[94:97]
	v_mfma_i32_16x16x64_i8 v[90:93], v[142:145], v[166:169], v[90:93]
	v_mfma_i32_16x16x64_i8 v[86:89], v[118:121], v[174:177], v[86:89]
	v_mfma_i32_16x16x64_i8 v[82:85], v[142:145], v[174:177], v[82:85]
	v_mfma_i32_16x16x64_i8 v[78:81], v[118:121], v[182:185], v[78:81]
	v_mfma_i32_16x16x64_i8 v[74:77], v[142:145], v[182:185], v[74:77]
	v_mfma_i32_16x16x64_i8 v[70:73], v[118:121], v[190:193], v[70:73]
	v_mfma_i32_16x16x64_i8 v[66:69], v[142:145], v[190:193], v[66:69]
	s_setprio 0
	s_setprio 1
	v_mfma_i32_16x16x64_i8 v[30:33], v[146:149], v[162:165], v[30:33]
	v_mfma_i32_16x16x64_i8 v[26:29], v[154:157], v[162:165], v[26:29]
	v_mfma_i32_16x16x64_i8 v[22:25], v[146:149], v[170:173], v[22:25]
	v_mfma_i32_16x16x64_i8 v[18:21], v[154:157], v[170:173], v[18:21]
	v_mfma_i32_16x16x64_i8 v[14:17], v[146:149], v[178:181], v[14:17]
	v_mfma_i32_16x16x64_i8 v[10:13], v[154:157], v[178:181], v[10:13]
	v_mfma_i32_16x16x64_i8 v[6:9], v[146:149], v[186:189], v[6:9]
	v_mfma_i32_16x16x64_i8 v[2:5], v[154:157], v[186:189], v[2:5]
	v_mfma_i32_16x16x64_i8 v[30:33], v[150:153], v[166:169], v[30:33]
	v_mfma_i32_16x16x64_i8 v[26:29], v[158:161], v[166:169], v[26:29]
	v_mfma_i32_16x16x64_i8 v[22:25], v[150:153], v[174:177], v[22:25]
	v_mfma_i32_16x16x64_i8 v[18:21], v[158:161], v[174:177], v[18:21]
	v_mfma_i32_16x16x64_i8 v[14:17], v[150:153], v[182:185], v[14:17]
	v_mfma_i32_16x16x64_i8 v[10:13], v[158:161], v[182:185], v[10:13]
	v_mfma_i32_16x16x64_i8 v[6:9], v[150:153], v[190:193], v[6:9]
	v_mfma_i32_16x16x64_i8 v[2:5], v[158:161], v[190:193], v[2:5]
	s_setprio 0
	s_barrier
	s_add_i32 s51, 0, 0x18000
	v_add_u32_e32 v0, s51, v198
	s_add_i32 s52, 0, 0x1c000
	ds_read_b128 v[114:117], v0
	ds_read_b128 v[118:121], v0 offset:1024
	ds_read_b128 v[138:141], v0 offset:2048
	ds_read_b128 v[142:145], v0 offset:3072
	v_add_u32_e32 v0, s52, v198
	ds_read_b128 v[146:149], v0
	ds_read_b128 v[150:153], v0 offset:1024
	ds_read_b128 v[154:157], v0 offset:2048
	ds_read_b128 v[158:161], v0 offset:3072
	s_add_u32 s54, s28, 0x20000
	ds_read_b128 v[162:165], v199 offset:32768
	ds_read_b128 v[166:169], v199 offset:33792
	ds_read_b128 v[170:173], v199 offset:34816
	ds_read_b128 v[174:177], v199 offset:35840
	ds_read_b128 v[178:181], v199 offset:36864
	ds_read_b128 v[182:185], v199 offset:37888
	ds_read_b128 v[186:189], v199 offset:38912
	ds_read_b128 v[190:193], v199 offset:39936
	s_addc_u32 s55, s29, 0
	v_mov_b32_e32 v0, v194
	s_mov_b32 m0, s85
	s_nop 0
	global_load_lds_dwordx4 v0, s[28:29]
	v_mov_b32_e32 v0, v196
	s_mov_b32 m0, s38
	s_nop 0
	global_load_lds_dwordx4 v0, s[28:29]
	v_mov_b32_e32 v0, v194
	s_mov_b32 m0, s39
	s_nop 0
	global_load_lds_dwordx4 v0, s[54:55]
	v_mov_b32_e32 v0, v196
	s_mov_b32 m0, s40
	s_nop 0
	global_load_lds_dwordx4 v0, s[54:55]
	s_waitcnt vmcnt(8)
	s_waitcnt lgkmcnt(0)
	s_barrier
	s_setprio 1
	s_waitcnt lgkmcnt(0)
	v_mfma_i32_16x16x64_i8 v[134:137], v[114:117], v[162:165], v[134:137]
	v_mfma_i32_16x16x64_i8 v[130:133], v[138:141], v[162:165], v[130:133]
	v_mfma_i32_16x16x64_i8 v[126:129], v[114:117], v[170:173], v[126:129]
	v_mfma_i32_16x16x64_i8 v[122:125], v[138:141], v[170:173], v[122:125]
	v_mfma_i32_16x16x64_i8 v[110:113], v[114:117], v[178:181], v[110:113]
	v_mfma_i32_16x16x64_i8 v[106:109], v[138:141], v[178:181], v[106:109]
	v_mfma_i32_16x16x64_i8 v[102:105], v[114:117], v[186:189], v[102:105]
	v_mfma_i32_16x16x64_i8 v[98:101], v[138:141], v[186:189], v[98:101]
	v_mfma_i32_16x16x64_i8 v[134:137], v[118:121], v[166:169], v[134:137]
	v_mfma_i32_16x16x64_i8 v[130:133], v[142:145], v[166:169], v[130:133]
	v_mfma_i32_16x16x64_i8 v[126:129], v[118:121], v[174:177], v[126:129]
	v_mfma_i32_16x16x64_i8 v[122:125], v[142:145], v[174:177], v[122:125]
	v_mfma_i32_16x16x64_i8 v[110:113], v[118:121], v[182:185], v[110:113]
	v_mfma_i32_16x16x64_i8 v[106:109], v[142:145], v[182:185], v[106:109]
	v_mfma_i32_16x16x64_i8 v[102:105], v[118:121], v[190:193], v[102:105]
	v_mfma_i32_16x16x64_i8 v[98:101], v[142:145], v[190:193], v[98:101]
	s_setprio 0
	s_setprio 1
	v_mfma_i32_16x16x64_i8 v[62:65], v[146:149], v[162:165], v[62:65]
	v_mfma_i32_16x16x64_i8 v[58:61], v[154:157], v[162:165], v[58:61]
	v_mfma_i32_16x16x64_i8 v[54:57], v[146:149], v[170:173], v[54:57]
	v_mfma_i32_16x16x64_i8 v[50:53], v[154:157], v[170:173], v[50:53]
	v_mfma_i32_16x16x64_i8 v[46:49], v[146:149], v[178:181], v[46:49]
	v_mfma_i32_16x16x64_i8 v[42:45], v[154:157], v[178:181], v[42:45]
	v_mfma_i32_16x16x64_i8 v[38:41], v[146:149], v[186:189], v[38:41]
	v_mfma_i32_16x16x64_i8 v[34:37], v[154:157], v[186:189], v[34:37]
	v_mfma_i32_16x16x64_i8 v[62:65], v[150:153], v[166:169], v[62:65]
	v_mfma_i32_16x16x64_i8 v[58:61], v[158:161], v[166:169], v[58:61]
	v_mfma_i32_16x16x64_i8 v[54:57], v[150:153], v[174:177], v[54:57]
	v_mfma_i32_16x16x64_i8 v[50:53], v[158:161], v[174:177], v[50:53]
	v_mfma_i32_16x16x64_i8 v[46:49], v[150:153], v[182:185], v[46:49]
	v_mfma_i32_16x16x64_i8 v[42:45], v[158:161], v[182:185], v[42:45]
	v_mfma_i32_16x16x64_i8 v[38:41], v[150:153], v[190:193], v[38:41]
	v_mfma_i32_16x16x64_i8 v[34:37], v[158:161], v[190:193], v[34:37]
	s_setprio 0
	s_barrier
	v_mov_b32_e32 v0, v195
	ds_read_b128 v[162:165], v199 offset:49152
	ds_read_b128 v[166:169], v199 offset:50176
	ds_read_b128 v[170:173], v199 offset:51200
	ds_read_b128 v[174:177], v199 offset:52224
	ds_read_b128 v[178:181], v199 offset:53248
	ds_read_b128 v[182:185], v199 offset:54272
	ds_read_b128 v[186:189], v199 offset:55296
	ds_read_b128 v[190:193], v199 offset:56320
	s_add_i32 s53, s51, s33
	v_lshl_add_u64 v[200:201], s[30:31], 0, v[0:1]
	v_lshl_add_u64 v[200:201], v[200:201], 0, s[90:91]
	s_mov_b32 m0, s53
	v_mov_b32_e32 v0, v197
	s_add_i32 s54, s53, 0x2000
	global_load_lds_dwordx4 v[200:201], off
	s_mov_b32 m0, s54
	v_lshl_add_u64 v[200:201], s[30:31], 0, v[0:1]
	s_add_u32 s30, s30, 0x20080
	v_lshl_add_u64 v[200:201], v[200:201], 0, s[90:91]
	s_addc_u32 s31, s31, 0
	v_mov_b32_e32 v0, v195
	s_add_i32 s55, s52, s33
	global_load_lds_dwordx4 v[200:201], off
	s_mov_b32 m0, s55
	s_add_i32 s56, s55, 0x2000
	global_load_lds_dwordx4 v0, s[30:31]
	v_mov_b32_e32 v0, v197
	s_mov_b32 m0, s56
	s_nop 0
	global_load_lds_dwordx4 v0, s[30:31]
	s_waitcnt vmcnt(6)
	s_waitcnt lgkmcnt(0)
	s_barrier
	s_setprio 1
	s_waitcnt lgkmcnt(0)
	v_mfma_i32_16x16x64_i8 v[94:97], v[114:117], v[162:165], v[94:97]
	v_mfma_i32_16x16x64_i8 v[90:93], v[138:141], v[162:165], v[90:93]
	v_mfma_i32_16x16x64_i8 v[86:89], v[114:117], v[170:173], v[86:89]
	v_mfma_i32_16x16x64_i8 v[82:85], v[138:141], v[170:173], v[82:85]
	v_mfma_i32_16x16x64_i8 v[78:81], v[114:117], v[178:181], v[78:81]
	v_mfma_i32_16x16x64_i8 v[74:77], v[138:141], v[178:181], v[74:77]
	v_mfma_i32_16x16x64_i8 v[70:73], v[114:117], v[186:189], v[70:73]
	v_mfma_i32_16x16x64_i8 v[66:69], v[138:141], v[186:189], v[66:69]
	v_mfma_i32_16x16x64_i8 v[94:97], v[118:121], v[166:169], v[94:97]
	v_mfma_i32_16x16x64_i8 v[90:93], v[142:145], v[166:169], v[90:93]
	v_mfma_i32_16x16x64_i8 v[86:89], v[118:121], v[174:177], v[86:89]
	v_mfma_i32_16x16x64_i8 v[82:85], v[142:145], v[174:177], v[82:85]
	v_mfma_i32_16x16x64_i8 v[78:81], v[118:121], v[182:185], v[78:81]
	v_mfma_i32_16x16x64_i8 v[74:77], v[142:145], v[182:185], v[74:77]
	v_mfma_i32_16x16x64_i8 v[70:73], v[118:121], v[190:193], v[70:73]
	v_mfma_i32_16x16x64_i8 v[66:69], v[142:145], v[190:193], v[66:69]
	s_setprio 0
	s_setprio 1
	v_mfma_i32_16x16x64_i8 v[30:33], v[146:149], v[162:165], v[30:33]
	v_mfma_i32_16x16x64_i8 v[26:29], v[154:157], v[162:165], v[26:29]
	v_mfma_i32_16x16x64_i8 v[22:25], v[146:149], v[170:173], v[22:25]
	v_mfma_i32_16x16x64_i8 v[18:21], v[154:157], v[170:173], v[18:21]
	v_mfma_i32_16x16x64_i8 v[14:17], v[146:149], v[178:181], v[14:17]
	v_mfma_i32_16x16x64_i8 v[10:13], v[154:157], v[178:181], v[10:13]
	v_mfma_i32_16x16x64_i8 v[6:9], v[146:149], v[186:189], v[6:9]
	v_mfma_i32_16x16x64_i8 v[2:5], v[154:157], v[186:189], v[2:5]
	v_mfma_i32_16x16x64_i8 v[30:33], v[150:153], v[166:169], v[30:33]
	v_mfma_i32_16x16x64_i8 v[26:29], v[158:161], v[166:169], v[26:29]
	v_mfma_i32_16x16x64_i8 v[22:25], v[150:153], v[174:177], v[22:25]
	v_mfma_i32_16x16x64_i8 v[18:21], v[158:161], v[174:177], v[18:21]
	v_mfma_i32_16x16x64_i8 v[14:17], v[150:153], v[182:185], v[14:17]
	v_mfma_i32_16x16x64_i8 v[10:13], v[158:161], v[182:185], v[10:13]
	v_mfma_i32_16x16x64_i8 v[6:9], v[150:153], v[190:193], v[6:9]
	v_mfma_i32_16x16x64_i8 v[2:5], v[158:161], v[190:193], v[2:5]
	s_setprio 0
	s_barrier
	v_mov_b32_e32 v0, v194
	s_mov_b32 m0, s41
	v_lshl_add_u64 v[192:193], s[28:29], 0, v[0:1]
	v_lshl_add_u64 v[192:193], v[192:193], 0, s[90:91]
	v_mov_b32_e32 v0, v196
	global_load_lds_dwordx4 v[192:193], off
	s_mov_b32 m0, s42
	v_lshl_add_u64 v[192:193], s[28:29], 0, v[0:1]
	v_lshl_add_u64 v[192:193], v[192:193], 0, s[90:91]
	global_load_lds_dwordx4 v[192:193], off
	s_add_i32 s68, s68, 2
	s_add_u32 s8, s8, 0x100
	s_addc_u32 s9, s9, 0
	s_add_u32 s66, s66, 0x100
	s_addc_u32 s67, s67, 0
	s_cmp_gt_u32 s68, 5
	s_cbranch_scc0 .LBB0_775
	v_readlane_b32 s8, v254, 19
	v_readlane_b32 s9, v254, 20
	s_and_b64 vcc, exec, s[8:9]
	s_cbranch_vccz .LBB0_778
	s_barrier

.LBB0_866:
	v_add_u32_e32 v0, s43, v248
	ds_read_b128 v[66:69], v0
	ds_read_b128 v[70:73], v0 offset:1024
	ds_read_b128 v[82:85], v0 offset:2048
	ds_read_b128 v[86:89], v0 offset:3072
	v_add_u32_e32 v0, s44, v248
	ds_read_b128 v[106:109], v0
	ds_read_b128 v[110:113], v0 offset:1024
	ds_read_b128 v[122:125], v0 offset:2048
	ds_read_b128 v[130:133], v0 offset:3072
	s_add_u32 s12, s10, 0xfff70080
	s_addc_u32 s13, s11, -1
	s_cmp_eq_u32 s66, 2
	s_cselect_b32 s13, s27, s13
	s_cselect_b32 s12, s26, s12
	s_cselect_b32 s15, s25, s65
	s_cselect_b32 s14, s24, s29
	v_mov_b32_e32 v0, v244
	s_mov_b32 m0, s45
	ds_read_b128 v[162:165], v249
	ds_read_b128 v[166:169], v249 offset:1024
	ds_read_b128 v[170:173], v249 offset:2048
	ds_read_b128 v[174:177], v249 offset:3072
	ds_read_b128 v[178:181], v249 offset:4096
	ds_read_b128 v[182:185], v249 offset:5120
	ds_read_b128 v[186:189], v249 offset:6144
	ds_read_b128 v[190:193], v249 offset:7168
	s_nop 0
	global_load_lds_dwordx4 v0, s[10:11]
	v_mov_b32_e32 v0, v246
	s_mov_b32 m0, s46
	s_nop 0
	global_load_lds_dwordx4 v0, s[10:11]
	s_waitcnt vmcnt(8)
	s_waitcnt lgkmcnt(0)
	s_barrier
	s_setprio 1
	s_waitcnt lgkmcnt(0)
	v_mfma_f32_16x16x32_bf16 v[158:161], v[66:69], v[162:165], v[158:161]
	v_mfma_f32_16x16x32_bf16 v[154:157], v[82:85], v[162:165], v[154:157]
	v_mfma_f32_16x16x32_bf16 v[142:145], v[66:69], v[170:173], v[142:145]
	v_mfma_f32_16x16x32_bf16 v[138:141], v[82:85], v[170:173], v[138:141]
	v_mfma_f32_16x16x32_bf16 v[118:121], v[66:69], v[178:181], v[118:121]
	v_mfma_f32_16x16x32_bf16 v[114:117], v[82:85], v[178:181], v[114:117]
	v_mfma_f32_16x16x32_bf16 v[94:97], v[66:69], v[186:189], v[94:97]
	v_mfma_f32_16x16x32_bf16 v[90:93], v[82:85], v[186:189], v[90:93]
	v_mfma_f32_16x16x32_bf16 v[158:161], v[70:73], v[166:169], v[158:161]
	v_mfma_f32_16x16x32_bf16 v[154:157], v[86:89], v[166:169], v[154:157]
	v_mfma_f32_16x16x32_bf16 v[142:145], v[70:73], v[174:177], v[142:145]
	v_mfma_f32_16x16x32_bf16 v[138:141], v[86:89], v[174:177], v[138:141]
	v_mfma_f32_16x16x32_bf16 v[118:121], v[70:73], v[182:185], v[118:121]
	v_mfma_f32_16x16x32_bf16 v[114:117], v[86:89], v[182:185], v[114:117]
	v_mfma_f32_16x16x32_bf16 v[94:97], v[70:73], v[190:193], v[94:97]
	v_mfma_f32_16x16x32_bf16 v[90:93], v[86:89], v[190:193], v[90:93]
	s_setprio 0
	s_setprio 1
	v_mfma_f32_16x16x32_bf16 v[150:153], v[106:109], v[162:165], v[150:153]
	v_mfma_f32_16x16x32_bf16 v[146:149], v[122:125], v[162:165], v[146:149]
	v_mfma_f32_16x16x32_bf16 v[134:137], v[106:109], v[170:173], v[134:137]
	v_mfma_f32_16x16x32_bf16 v[126:129], v[122:125], v[170:173], v[126:129]
	v_mfma_f32_16x16x32_bf16 v[102:105], v[106:109], v[178:181], v[102:105]
	v_mfma_f32_16x16x32_bf16 v[98:101], v[122:125], v[178:181], v[98:101]
	v_mfma_f32_16x16x32_bf16 v[78:81], v[106:109], v[186:189], v[78:81]
	v_mfma_f32_16x16x32_bf16 v[74:77], v[122:125], v[186:189], v[74:77]
	v_mfma_f32_16x16x32_bf16 v[150:153], v[110:113], v[166:169], v[150:153]
	v_mfma_f32_16x16x32_bf16 v[146:149], v[130:133], v[166:169], v[146:149]
	v_mfma_f32_16x16x32_bf16 v[134:137], v[110:113], v[174:177], v[134:137]
	v_mfma_f32_16x16x32_bf16 v[126:129], v[130:133], v[174:177], v[126:129]
	v_mfma_f32_16x16x32_bf16 v[102:105], v[110:113], v[182:185], v[102:105]
	v_mfma_f32_16x16x32_bf16 v[98:101], v[130:133], v[182:185], v[98:101]
	v_mfma_f32_16x16x32_bf16 v[78:81], v[110:113], v[190:193], v[78:81]
	v_mfma_f32_16x16x32_bf16 v[74:77], v[130:133], v[190:193], v[74:77]
	s_setprio 0
	s_barrier
	v_mov_b32_e32 v0, v245
	s_mov_b32 m0, s47
	ds_read_b128 v[162:165], v249 offset:16384
	ds_read_b128 v[166:169], v249 offset:17408
	ds_read_b128 v[170:173], v249 offset:18432
	ds_read_b128 v[174:177], v249 offset:19456
	ds_read_b128 v[178:181], v249 offset:20480
	ds_read_b128 v[182:185], v249 offset:21504
	ds_read_b128 v[186:189], v249 offset:22528
	ds_read_b128 v[190:193], v249 offset:23552
	s_add_u32 s68, s14, 0x18000
	global_load_lds_dwordx4 v0, s[14:15]
	v_mov_b32_e32 v0, v247
	s_mov_b32 m0, s48
	s_addc_u32 s69, s15, 0
	global_load_lds_dwordx4 v0, s[14:15]
	v_mov_b32_e32 v0, v245
	s_mov_b32 m0, s49
	s_nop 0
	global_load_lds_dwordx4 v0, s[68:69]
	v_mov_b32_e32 v0, v247
	s_mov_b32 m0, s50
	s_nop 0
	global_load_lds_dwordx4 v0, s[68:69]
	s_waitcnt vmcnt(6)
	s_waitcnt lgkmcnt(0)
	s_barrier
	s_setprio 1
	s_waitcnt lgkmcnt(0)
	v_mfma_f32_16x16x32_bf16 v[62:65], v[66:69], v[162:165], v[62:65]
	v_mfma_f32_16x16x32_bf16 v[58:61], v[82:85], v[162:165], v[58:61]
	v_mfma_f32_16x16x32_bf16 v[46:49], v[66:69], v[170:173], v[46:49]
	v_mfma_f32_16x16x32_bf16 v[42:45], v[82:85], v[170:173], v[42:45]
	v_mfma_f32_16x16x32_bf16 v[30:33], v[66:69], v[178:181], v[30:33]
	v_mfma_f32_16x16x32_bf16 v[26:29], v[82:85], v[178:181], v[26:29]
	v_mfma_f32_16x16x32_bf16 v[14:17], v[66:69], v[186:189], v[14:17]
	v_mfma_f32_16x16x32_bf16 v[10:13], v[82:85], v[186:189], v[10:13]
	v_mfma_f32_16x16x32_bf16 v[62:65], v[70:73], v[166:169], v[62:65]
	v_mfma_f32_16x16x32_bf16 v[58:61], v[86:89], v[166:169], v[58:61]
	v_mfma_f32_16x16x32_bf16 v[46:49], v[70:73], v[174:177], v[46:49]
	v_mfma_f32_16x16x32_bf16 v[42:45], v[86:89], v[174:177], v[42:45]
	v_mfma_f32_16x16x32_bf16 v[30:33], v[70:73], v[182:185], v[30:33]
	v_mfma_f32_16x16x32_bf16 v[26:29], v[86:89], v[182:185], v[26:29]
	v_mfma_f32_16x16x32_bf16 v[14:17], v[70:73], v[190:193], v[14:17]
	v_mfma_f32_16x16x32_bf16 v[10:13], v[86:89], v[190:193], v[10:13]
	s_setprio 0
	s_setprio 1
	v_mfma_f32_16x16x32_bf16 v[54:57], v[106:109], v[162:165], v[54:57]
	v_mfma_f32_16x16x32_bf16 v[50:53], v[122:125], v[162:165], v[50:53]
	v_mfma_f32_16x16x32_bf16 v[38:41], v[106:109], v[170:173], v[38:41]
	v_mfma_f32_16x16x32_bf16 v[34:37], v[122:125], v[170:173], v[34:37]
	v_mfma_f32_16x16x32_bf16 v[22:25], v[106:109], v[178:181], v[22:25]
	v_mfma_f32_16x16x32_bf16 v[18:21], v[122:125], v[178:181], v[18:21]
	v_mfma_f32_16x16x32_bf16 v[6:9], v[106:109], v[186:189], v[6:9]
	v_mfma_f32_16x16x32_bf16 v[2:5], v[122:125], v[186:189], v[2:5]
	v_mfma_f32_16x16x32_bf16 v[54:57], v[110:113], v[166:169], v[54:57]
	v_mfma_f32_16x16x32_bf16 v[50:53], v[130:133], v[166:169], v[50:53]
	v_mfma_f32_16x16x32_bf16 v[38:41], v[110:113], v[174:177], v[38:41]
	v_mfma_f32_16x16x32_bf16 v[34:37], v[130:133], v[174:177], v[34:37]
	v_mfma_f32_16x16x32_bf16 v[22:25], v[110:113], v[182:185], v[22:25]
	v_mfma_f32_16x16x32_bf16 v[18:21], v[130:133], v[182:185], v[18:21]
	v_mfma_f32_16x16x32_bf16 v[6:9], v[110:113], v[190:193], v[6:9]
	v_mfma_f32_16x16x32_bf16 v[2:5], v[130:133], v[190:193], v[2:5]
	s_setprio 0
	s_barrier
	v_add_u32_e32 v0, s51, v248
	ds_read_b128 v[66:69], v0
	ds_read_b128 v[70:73], v0 offset:1024
	ds_read_b128 v[82:85], v0 offset:2048
	ds_read_b128 v[86:89], v0 offset:3072
	v_add_u32_e32 v0, s52, v248
	ds_read_b128 v[106:109], v0
	ds_read_b128 v[110:113], v0 offset:1024
	ds_read_b128 v[122:125], v0 offset:2048
	ds_read_b128 v[130:133], v0 offset:3072
	s_add_u32 s68, s12, 0x90000
	ds_read_b128 v[162:165], v249 offset:32768
	ds_read_b128 v[166:169], v249 offset:33792
	ds_read_b128 v[170:173], v249 offset:34816
	ds_read_b128 v[174:177], v249 offset:35840
	ds_read_b128 v[178:181], v249 offset:36864
	ds_read_b128 v[182:185], v249 offset:37888
	ds_read_b128 v[186:189], v249 offset:38912
	ds_read_b128 v[190:193], v249 offset:39936
	s_addc_u32 s69, s13, 0
	v_mov_b32_e32 v0, v244
	s_mov_b32 m0, s85
	s_nop 0
	global_load_lds_dwordx4 v0, s[12:13]
	v_mov_b32_e32 v0, v246
	s_mov_b32 m0, s38
	s_nop 0
	global_load_lds_dwordx4 v0, s[12:13]
	v_mov_b32_e32 v0, v244
	s_mov_b32 m0, s39
	s_nop 0
	global_load_lds_dwordx4 v0, s[68:69]
	v_mov_b32_e32 v0, v246
	s_mov_b32 m0, s40
	s_nop 0
	global_load_lds_dwordx4 v0, s[68:69]
	s_waitcnt vmcnt(8)
	s_waitcnt lgkmcnt(0)
	s_barrier
	s_setprio 1
	s_waitcnt lgkmcnt(0)
	v_mfma_f32_16x16x32_bf16 v[158:161], v[66:69], v[162:165], v[158:161]
	v_mfma_f32_16x16x32_bf16 v[154:157], v[82:85], v[162:165], v[154:157]
	v_mfma_f32_16x16x32_bf16 v[142:145], v[66:69], v[170:173], v[142:145]
	v_mfma_f32_16x16x32_bf16 v[138:141], v[82:85], v[170:173], v[138:141]
	v_mfma_f32_16x16x32_bf16 v[118:121], v[66:69], v[178:181], v[118:121]
	v_mfma_f32_16x16x32_bf16 v[114:117], v[82:85], v[178:181], v[114:117]
	v_mfma_f32_16x16x32_bf16 v[94:97], v[66:69], v[186:189], v[94:97]
	v_mfma_f32_16x16x32_bf16 v[90:93], v[82:85], v[186:189], v[90:93]
	v_mfma_f32_16x16x32_bf16 v[158:161], v[70:73], v[166:169], v[158:161]
	v_mfma_f32_16x16x32_bf16 v[154:157], v[86:89], v[166:169], v[154:157]
	v_mfma_f32_16x16x32_bf16 v[142:145], v[70:73], v[174:177], v[142:145]
	v_mfma_f32_16x16x32_bf16 v[138:141], v[86:89], v[174:177], v[138:141]
	v_mfma_f32_16x16x32_bf16 v[118:121], v[70:73], v[182:185], v[118:121]
	v_mfma_f32_16x16x32_bf16 v[114:117], v[86:89], v[182:185], v[114:117]
	v_mfma_f32_16x16x32_bf16 v[94:97], v[70:73], v[190:193], v[94:97]
	v_mfma_f32_16x16x32_bf16 v[90:93], v[86:89], v[190:193], v[90:93]
	s_setprio 0
	s_setprio 1
	v_mfma_f32_16x16x32_bf16 v[150:153], v[106:109], v[162:165], v[150:153]
	v_mfma_f32_16x16x32_bf16 v[146:149], v[122:125], v[162:165], v[146:149]
	v_mfma_f32_16x16x32_bf16 v[134:137], v[106:109], v[170:173], v[134:137]
	v_mfma_f32_16x16x32_bf16 v[126:129], v[122:125], v[170:173], v[126:129]
	v_mfma_f32_16x16x32_bf16 v[102:105], v[106:109], v[178:181], v[102:105]
	v_mfma_f32_16x16x32_bf16 v[98:101], v[122:125], v[178:181], v[98:101]
	v_mfma_f32_16x16x32_bf16 v[78:81], v[106:109], v[186:189], v[78:81]
	v_mfma_f32_16x16x32_bf16 v[74:77], v[122:125], v[186:189], v[74:77]
	v_mfma_f32_16x16x32_bf16 v[150:153], v[110:113], v[166:169], v[150:153]
	v_mfma_f32_16x16x32_bf16 v[146:149], v[130:133], v[166:169], v[146:149]
	v_mfma_f32_16x16x32_bf16 v[134:137], v[110:113], v[174:177], v[134:137]
	v_mfma_f32_16x16x32_bf16 v[126:129], v[130:133], v[174:177], v[126:129]
	v_mfma_f32_16x16x32_bf16 v[102:105], v[110:113], v[182:185], v[102:105]
	v_mfma_f32_16x16x32_bf16 v[98:101], v[130:133], v[182:185], v[98:101]
	v_mfma_f32_16x16x32_bf16 v[78:81], v[110:113], v[190:193], v[78:81]
	v_mfma_f32_16x16x32_bf16 v[74:77], v[130:133], v[190:193], v[74:77]
	s_setprio 0
	s_barrier
	v_mov_b32_e32 v0, v245
	ds_read_b128 v[162:165], v249 offset:49152
	ds_read_b128 v[166:169], v249 offset:50176
	ds_read_b128 v[170:173], v249 offset:51200
	ds_read_b128 v[174:177], v249 offset:52224
	ds_read_b128 v[178:181], v249 offset:53248
	ds_read_b128 v[182:185], v249 offset:54272
	ds_read_b128 v[186:189], v249 offset:55296
	ds_read_b128 v[190:193], v249 offset:56320
	s_mov_b32 m0, s53
	v_lshl_add_u64 v[194:195], s[14:15], 0, v[0:1]
	v_lshl_add_u64 v[194:195], v[194:195], 0, s[90:91]
	v_mov_b32_e32 v0, v247
	global_load_lds_dwordx4 v[194:195], off
	s_mov_b32 m0, s54
	v_lshl_add_u64 v[194:195], s[14:15], 0, v[0:1]
	v_lshl_add_u64 v[194:195], v[194:195], 0, s[90:91]
	s_add_u32 s14, s14, 0x18080
	v_mov_b32_e32 v0, v245
	global_load_lds_dwordx4 v[194:195], off
	s_addc_u32 s15, s15, 0
	s_mov_b32 m0, s55
	s_nop 0
	global_load_lds_dwordx4 v0, s[14:15]
	v_mov_b32_e32 v0, v247
	s_mov_b32 m0, s56
	s_nop 0
	global_load_lds_dwordx4 v0, s[14:15]
	s_waitcnt vmcnt(6)
	s_waitcnt lgkmcnt(0)
	s_barrier
	s_setprio 1
	s_waitcnt lgkmcnt(0)
	v_mfma_f32_16x16x32_bf16 v[62:65], v[66:69], v[162:165], v[62:65]
	v_mfma_f32_16x16x32_bf16 v[58:61], v[82:85], v[162:165], v[58:61]
	v_mfma_f32_16x16x32_bf16 v[46:49], v[66:69], v[170:173], v[46:49]
	v_mfma_f32_16x16x32_bf16 v[42:45], v[82:85], v[170:173], v[42:45]
	v_mfma_f32_16x16x32_bf16 v[30:33], v[66:69], v[178:181], v[30:33]
	v_mfma_f32_16x16x32_bf16 v[26:29], v[82:85], v[178:181], v[26:29]
	v_mfma_f32_16x16x32_bf16 v[14:17], v[66:69], v[186:189], v[14:17]
	v_mfma_f32_16x16x32_bf16 v[10:13], v[82:85], v[186:189], v[10:13]
	v_mfma_f32_16x16x32_bf16 v[62:65], v[70:73], v[166:169], v[62:65]
	v_mfma_f32_16x16x32_bf16 v[58:61], v[86:89], v[166:169], v[58:61]
	v_mfma_f32_16x16x32_bf16 v[46:49], v[70:73], v[174:177], v[46:49]
	v_mfma_f32_16x16x32_bf16 v[42:45], v[86:89], v[174:177], v[42:45]
	v_mfma_f32_16x16x32_bf16 v[30:33], v[70:73], v[182:185], v[30:33]
	v_mfma_f32_16x16x32_bf16 v[26:29], v[86:89], v[182:185], v[26:29]
	v_mfma_f32_16x16x32_bf16 v[14:17], v[70:73], v[190:193], v[14:17]
	v_mfma_f32_16x16x32_bf16 v[10:13], v[86:89], v[190:193], v[10:13]
	s_setprio 0
	s_setprio 1
	v_mfma_f32_16x16x32_bf16 v[54:57], v[106:109], v[162:165], v[54:57]
	v_mfma_f32_16x16x32_bf16 v[50:53], v[122:125], v[162:165], v[50:53]
	v_mfma_f32_16x16x32_bf16 v[38:41], v[106:109], v[170:173], v[38:41]
	v_mfma_f32_16x16x32_bf16 v[34:37], v[122:125], v[170:173], v[34:37]
	v_mfma_f32_16x16x32_bf16 v[22:25], v[106:109], v[178:181], v[22:25]
	v_mfma_f32_16x16x32_bf16 v[18:21], v[122:125], v[178:181], v[18:21]
	v_mfma_f32_16x16x32_bf16 v[6:9], v[106:109], v[186:189], v[6:9]
	v_mfma_f32_16x16x32_bf16 v[2:5], v[122:125], v[186:189], v[2:5]
	v_mfma_f32_16x16x32_bf16 v[54:57], v[110:113], v[166:169], v[54:57]
	v_mfma_f32_16x16x32_bf16 v[50:53], v[130:133], v[166:169], v[50:53]
	v_mfma_f32_16x16x32_bf16 v[38:41], v[110:113], v[174:177], v[38:41]
	v_mfma_f32_16x16x32_bf16 v[34:37], v[130:133], v[174:177], v[34:37]
	v_mfma_f32_16x16x32_bf16 v[22:25], v[110:113], v[182:185], v[22:25]
	v_mfma_f32_16x16x32_bf16 v[18:21], v[130:133], v[182:185], v[18:21]
	v_mfma_f32_16x16x32_bf16 v[6:9], v[110:113], v[190:193], v[6:9]
	v_mfma_f32_16x16x32_bf16 v[2:5], v[130:133], v[190:193], v[2:5]
	s_setprio 0
	s_barrier
	v_mov_b32_e32 v0, v244
	s_mov_b32 m0, s41
	v_lshl_add_u64 v[194:195], s[12:13], 0, v[0:1]
	v_lshl_add_u64 v[194:195], v[194:195], 0, s[90:91]
	v_mov_b32_e32 v0, v246
	global_load_lds_dwordx4 v[194:195], off
	s_mov_b32 m0, s42
	v_lshl_add_u64 v[194:195], s[12:13], 0, v[0:1]
	v_lshl_add_u64 v[194:195], v[194:195], 0, s[90:91]
	global_load_lds_dwordx4 v[194:195], off
	s_add_i32 s66, s66, 2
	s_add_u32 s10, s10, 0x100
	s_addc_u32 s11, s11, 0
	s_add_u32 s29, s29, 0x100
	s_addc_u32 s65, s65, 0
	s_cmp_gt_u32 s66, 3
	s_cbranch_scc0 .LBB0_866
	v_readlane_b32 s10, v254, 19
	v_readlane_b32 s11, v254, 20
	s_and_b64 vcc, exec, s[10:11]
	s_cbranch_vccz .LBB0_869
	s_barrier

.LBB0_1200:
	s_add_u32 s30, s24, s12
	s_addc_u32 s31, s25, s13
	s_add_u32 s14, s30, 0x1f000100
	s_addc_u32 s15, s31, 0
	s_add_u32 s16, s26, s12
	s_addc_u32 s17, s27, s13
	s_add_i32 s29, 0, 0x10000
	s_cmpk_eq_i32 s12, 0x700
	s_cselect_b32 s15, s11, s15
	s_cselect_b32 s14, s10, s14
	v_add_u32_e32 v0, s29, v134
	s_cselect_b32 s17, s5, s17
	s_cselect_b32 s16, s4, s16
	s_add_i32 s34, 0, 0x14000
	ds_read_b128 v[136:139], v0
	ds_read_b128 v[140:143], v0 offset:1024
	ds_read_b128 v[144:147], v0 offset:2048
	ds_read_b128 v[148:151], v0 offset:3072
	v_add_u32_e32 v0, s34, v134
	ds_read_b128 v[152:155], v0
	ds_read_b128 v[156:159], v0 offset:1024
	ds_read_b128 v[160:163], v0 offset:2048
	ds_read_b128 v[164:167], v0 offset:3072
	v_mov_b32_e32 v0, v130
	ds_read_b128 v[168:171], v135
	ds_read_b128 v[172:175], v135 offset:1024
	ds_read_b128 v[176:179], v135 offset:2048
	ds_read_b128 v[180:183], v135 offset:3072
	ds_read_b128 v[184:187], v135 offset:4096
	ds_read_b128 v[188:191], v135 offset:5120
	ds_read_b128 v[192:195], v135 offset:6144
	ds_read_b128 v[196:199], v135 offset:7168
	s_add_i32 m0, s85, 0xc000
	v_lshl_add_u64 v[200:201], s[30:31], 0, v[0:1]
	v_lshl_add_u64 v[200:201], v[200:201], 0, s[64:65]
	v_mov_b32_e32 v0, v132
	global_load_lds_dwordx4 v[200:201], off
	s_add_i32 m0, s85, 0xe000
	v_lshl_add_u64 v[200:201], s[30:31], 0, v[0:1]
	v_lshl_add_u64 v[200:201], v[200:201], 0, s[64:65]
	global_load_lds_dwordx4 v[200:201], off
	s_waitcnt vmcnt(8)
	s_waitcnt lgkmcnt(0)
	s_barrier
	s_setprio 1
	s_waitcnt lgkmcnt(0)
	v_mfma_f32_16x16x32_bf16 v[126:129], v[136:139], v[168:171], v[126:129]
	v_mfma_f32_16x16x32_bf16 v[122:125], v[144:147], v[168:171], v[122:125]
	v_mfma_f32_16x16x32_bf16 v[118:121], v[136:139], v[176:179], v[118:121]
	v_mfma_f32_16x16x32_bf16 v[114:117], v[144:147], v[176:179], v[114:117]
	v_mfma_f32_16x16x32_bf16 v[110:113], v[136:139], v[184:187], v[110:113]
	v_mfma_f32_16x16x32_bf16 v[106:109], v[144:147], v[184:187], v[106:109]
	v_mfma_f32_16x16x32_bf16 v[102:105], v[136:139], v[192:195], v[102:105]
	v_mfma_f32_16x16x32_bf16 v[98:101], v[144:147], v[192:195], v[98:101]
	v_mfma_f32_16x16x32_bf16 v[126:129], v[140:143], v[172:175], v[126:129]
	v_mfma_f32_16x16x32_bf16 v[122:125], v[148:151], v[172:175], v[122:125]
	v_mfma_f32_16x16x32_bf16 v[118:121], v[140:143], v[180:183], v[118:121]
	v_mfma_f32_16x16x32_bf16 v[114:117], v[148:151], v[180:183], v[114:117]
	v_mfma_f32_16x16x32_bf16 v[110:113], v[140:143], v[188:191], v[110:113]
	v_mfma_f32_16x16x32_bf16 v[106:109], v[148:151], v[188:191], v[106:109]
	v_mfma_f32_16x16x32_bf16 v[102:105], v[140:143], v[196:199], v[102:105]
	v_mfma_f32_16x16x32_bf16 v[98:101], v[148:151], v[196:199], v[98:101]
	s_setprio 0
	s_setprio 1
	v_mfma_f32_16x16x32_bf16 v[62:65], v[152:155], v[168:171], v[62:65]
	v_mfma_f32_16x16x32_bf16 v[58:61], v[160:163], v[168:171], v[58:61]
	v_mfma_f32_16x16x32_bf16 v[54:57], v[152:155], v[176:179], v[54:57]
	v_mfma_f32_16x16x32_bf16 v[50:53], v[160:163], v[176:179], v[50:53]
	v_mfma_f32_16x16x32_bf16 v[46:49], v[152:155], v[184:187], v[46:49]
	v_mfma_f32_16x16x32_bf16 v[42:45], v[160:163], v[184:187], v[42:45]
	v_mfma_f32_16x16x32_bf16 v[38:41], v[152:155], v[192:195], v[38:41]
	v_mfma_f32_16x16x32_bf16 v[34:37], v[160:163], v[192:195], v[34:37]
	v_mfma_f32_16x16x32_bf16 v[62:65], v[156:159], v[172:175], v[62:65]
	v_mfma_f32_16x16x32_bf16 v[58:61], v[164:167], v[172:175], v[58:61]
	v_mfma_f32_16x16x32_bf16 v[54:57], v[156:159], v[180:183], v[54:57]
	v_mfma_f32_16x16x32_bf16 v[50:53], v[164:167], v[180:183], v[50:53]
	v_mfma_f32_16x16x32_bf16 v[46:49], v[156:159], v[188:191], v[46:49]
	v_mfma_f32_16x16x32_bf16 v[42:45], v[164:167], v[188:191], v[42:45]
	v_mfma_f32_16x16x32_bf16 v[38:41], v[156:159], v[196:199], v[38:41]
	v_mfma_f32_16x16x32_bf16 v[34:37], v[164:167], v[196:199], v[34:37]
	s_setprio 0
	s_barrier
	v_mov_b32_e32 v0, v131
	s_add_i32 s29, s29, s33
	ds_read_b128 v[168:171], v135 offset:16384
	ds_read_b128 v[172:175], v135 offset:17408
	ds_read_b128 v[176:179], v135 offset:18432
	ds_read_b128 v[180:183], v135 offset:19456
	ds_read_b128 v[184:187], v135 offset:20480
	ds_read_b128 v[188:191], v135 offset:21504
	ds_read_b128 v[192:195], v135 offset:22528
	ds_read_b128 v[196:199], v135 offset:23552
	s_mov_b32 m0, s29
	s_nop 0
	global_load_lds_dwordx4 v0, s[16:17]
	v_mov_b32_e32 v0, v133
	s_add_i32 m0, s29, 0x2000
	s_add_u32 s30, s16, 0x40000
	global_load_lds_dwordx4 v0, s[16:17]
	s_addc_u32 s31, s17, 0
	v_mov_b32_e32 v0, v131
	s_add_i32 s29, s34, s33
	s_mov_b32 m0, s29
	s_nop 0
	global_load_lds_dwordx4 v0, s[30:31]
	v_mov_b32_e32 v0, v133
	s_add_i32 m0, s29, 0x2000
	s_nop 0
	global_load_lds_dwordx4 v0, s[30:31]
	s_waitcnt vmcnt(6)
	s_waitcnt lgkmcnt(0)
	s_barrier
	s_setprio 1
	s_waitcnt lgkmcnt(0)
	v_mfma_f32_16x16x32_bf16 v[94:97], v[136:139], v[168:171], v[94:97]
	v_mfma_f32_16x16x32_bf16 v[90:93], v[144:147], v[168:171], v[90:93]
	v_mfma_f32_16x16x32_bf16 v[86:89], v[136:139], v[176:179], v[86:89]
	v_mfma_f32_16x16x32_bf16 v[82:85], v[144:147], v[176:179], v[82:85]
	v_mfma_f32_16x16x32_bf16 v[78:81], v[136:139], v[184:187], v[78:81]
	v_mfma_f32_16x16x32_bf16 v[74:77], v[144:147], v[184:187], v[74:77]
	v_mfma_f32_16x16x32_bf16 v[70:73], v[136:139], v[192:195], v[70:73]
	v_mfma_f32_16x16x32_bf16 v[66:69], v[144:147], v[192:195], v[66:69]
	v_mfma_f32_16x16x32_bf16 v[94:97], v[140:143], v[172:175], v[94:97]
	v_mfma_f32_16x16x32_bf16 v[90:93], v[148:151], v[172:175], v[90:93]
	v_mfma_f32_16x16x32_bf16 v[86:89], v[140:143], v[180:183], v[86:89]
	v_mfma_f32_16x16x32_bf16 v[82:85], v[148:151], v[180:183], v[82:85]
	v_mfma_f32_16x16x32_bf16 v[78:81], v[140:143], v[188:191], v[78:81]
	v_mfma_f32_16x16x32_bf16 v[74:77], v[148:151], v[188:191], v[74:77]
	v_mfma_f32_16x16x32_bf16 v[70:73], v[140:143], v[196:199], v[70:73]
	v_mfma_f32_16x16x32_bf16 v[66:69], v[148:151], v[196:199], v[66:69]
	s_setprio 0
	s_setprio 1
	v_mfma_f32_16x16x32_bf16 v[30:33], v[152:155], v[168:171], v[30:33]
	v_mfma_f32_16x16x32_bf16 v[26:29], v[160:163], v[168:171], v[26:29]
	v_mfma_f32_16x16x32_bf16 v[22:25], v[152:155], v[176:179], v[22:25]
	v_mfma_f32_16x16x32_bf16 v[18:21], v[160:163], v[176:179], v[18:21]
	v_mfma_f32_16x16x32_bf16 v[14:17], v[152:155], v[184:187], v[14:17]
	v_mfma_f32_16x16x32_bf16 v[10:13], v[160:163], v[184:187], v[10:13]
	v_mfma_f32_16x16x32_bf16 v[6:9], v[152:155], v[192:195], v[6:9]
	v_mfma_f32_16x16x32_bf16 v[2:5], v[160:163], v[192:195], v[2:5]
	v_mfma_f32_16x16x32_bf16 v[30:33], v[156:159], v[172:175], v[30:33]
	v_mfma_f32_16x16x32_bf16 v[26:29], v[164:167], v[172:175], v[26:29]
	v_mfma_f32_16x16x32_bf16 v[22:25], v[156:159], v[180:183], v[22:25]
	v_mfma_f32_16x16x32_bf16 v[18:21], v[164:167], v[180:183], v[18:21]
	v_mfma_f32_16x16x32_bf16 v[14:17], v[156:159], v[188:191], v[14:17]
	v_mfma_f32_16x16x32_bf16 v[10:13], v[164:167], v[188:191], v[10:13]
	v_mfma_f32_16x16x32_bf16 v[6:9], v[156:159], v[196:199], v[6:9]
	v_mfma_f32_16x16x32_bf16 v[2:5], v[164:167], v[196:199], v[2:5]
	s_setprio 0
	s_barrier
	s_add_i32 s29, 0, 0x18000
	v_add_u32_e32 v0, s29, v134
	s_add_i32 s34, 0, 0x1c000
	ds_read_b128 v[136:139], v0
	ds_read_b128 v[140:143], v0 offset:1024
	ds_read_b128 v[144:147], v0 offset:2048
	ds_read_b128 v[148:151], v0 offset:3072
	v_add_u32_e32 v0, s34, v134
	ds_read_b128 v[152:155], v0
	ds_read_b128 v[156:159], v0 offset:1024
	ds_read_b128 v[160:163], v0 offset:2048
	ds_read_b128 v[164:167], v0 offset:3072
	s_add_u32 s30, s14, 0x40000
	ds_read_b128 v[168:171], v135 offset:32768
	ds_read_b128 v[172:175], v135 offset:33792
	ds_read_b128 v[176:179], v135 offset:34816
	ds_read_b128 v[180:183], v135 offset:35840
	ds_read_b128 v[184:187], v135 offset:36864
	ds_read_b128 v[188:191], v135 offset:37888
	ds_read_b128 v[192:195], v135 offset:38912
	ds_read_b128 v[196:199], v135 offset:39936
	s_addc_u32 s31, s15, 0
	v_mov_b32_e32 v0, v130
	s_mov_b32 m0, s85
	s_nop 0
	global_load_lds_dwordx4 v0, s[14:15]
	v_mov_b32_e32 v0, v132
	s_mov_b32 m0, s9
	s_nop 0
	global_load_lds_dwordx4 v0, s[14:15]
	v_mov_b32_e32 v0, v130
	s_mov_b32 m0, s20
	s_nop 0
	global_load_lds_dwordx4 v0, s[30:31]
	v_mov_b32_e32 v0, v132
	s_mov_b32 m0, s21
	s_nop 0
	global_load_lds_dwordx4 v0, s[30:31]
	s_waitcnt vmcnt(8)
	s_waitcnt lgkmcnt(0)
	s_barrier
	s_setprio 1
	s_waitcnt lgkmcnt(0)
	v_mfma_f32_16x16x32_bf16 v[126:129], v[136:139], v[168:171], v[126:129]
	v_mfma_f32_16x16x32_bf16 v[122:125], v[144:147], v[168:171], v[122:125]
	v_mfma_f32_16x16x32_bf16 v[118:121], v[136:139], v[176:179], v[118:121]
	v_mfma_f32_16x16x32_bf16 v[114:117], v[144:147], v[176:179], v[114:117]
	v_mfma_f32_16x16x32_bf16 v[110:113], v[136:139], v[184:187], v[110:113]
	v_mfma_f32_16x16x32_bf16 v[106:109], v[144:147], v[184:187], v[106:109]
	v_mfma_f32_16x16x32_bf16 v[102:105], v[136:139], v[192:195], v[102:105]
	v_mfma_f32_16x16x32_bf16 v[98:101], v[144:147], v[192:195], v[98:101]
	v_mfma_f32_16x16x32_bf16 v[126:129], v[140:143], v[172:175], v[126:129]
	v_mfma_f32_16x16x32_bf16 v[122:125], v[148:151], v[172:175], v[122:125]
	v_mfma_f32_16x16x32_bf16 v[118:121], v[140:143], v[180:183], v[118:121]
	v_mfma_f32_16x16x32_bf16 v[114:117], v[148:151], v[180:183], v[114:117]
	v_mfma_f32_16x16x32_bf16 v[110:113], v[140:143], v[188:191], v[110:113]
	v_mfma_f32_16x16x32_bf16 v[106:109], v[148:151], v[188:191], v[106:109]
	v_mfma_f32_16x16x32_bf16 v[102:105], v[140:143], v[196:199], v[102:105]
	v_mfma_f32_16x16x32_bf16 v[98:101], v[148:151], v[196:199], v[98:101]
	s_setprio 0
	s_setprio 1
	v_mfma_f32_16x16x32_bf16 v[62:65], v[152:155], v[168:171], v[62:65]
	v_mfma_f32_16x16x32_bf16 v[58:61], v[160:163], v[168:171], v[58:61]
	v_mfma_f32_16x16x32_bf16 v[54:57], v[152:155], v[176:179], v[54:57]
	v_mfma_f32_16x16x32_bf16 v[50:53], v[160:163], v[176:179], v[50:53]
	v_mfma_f32_16x16x32_bf16 v[46:49], v[152:155], v[184:187], v[46:49]
	v_mfma_f32_16x16x32_bf16 v[42:45], v[160:163], v[184:187], v[42:45]
	v_mfma_f32_16x16x32_bf16 v[38:41], v[152:155], v[192:195], v[38:41]
	v_mfma_f32_16x16x32_bf16 v[34:37], v[160:163], v[192:195], v[34:37]
	v_mfma_f32_16x16x32_bf16 v[62:65], v[156:159], v[172:175], v[62:65]
	v_mfma_f32_16x16x32_bf16 v[58:61], v[164:167], v[172:175], v[58:61]
	v_mfma_f32_16x16x32_bf16 v[54:57], v[156:159], v[180:183], v[54:57]
	v_mfma_f32_16x16x32_bf16 v[50:53], v[164:167], v[180:183], v[50:53]
	v_mfma_f32_16x16x32_bf16 v[46:49], v[156:159], v[188:191], v[46:49]
	v_mfma_f32_16x16x32_bf16 v[42:45], v[164:167], v[188:191], v[42:45]
	v_mfma_f32_16x16x32_bf16 v[38:41], v[156:159], v[196:199], v[38:41]
	v_mfma_f32_16x16x32_bf16 v[34:37], v[164:167], v[196:199], v[34:37]
	s_setprio 0
	s_barrier
	v_mov_b32_e32 v0, v131
	ds_read_b128 v[168:171], v135 offset:49152
	ds_read_b128 v[172:175], v135 offset:50176
	ds_read_b128 v[176:179], v135 offset:51200
	ds_read_b128 v[180:183], v135 offset:52224
	ds_read_b128 v[184:187], v135 offset:53248
	ds_read_b128 v[188:191], v135 offset:54272
	ds_read_b128 v[192:195], v135 offset:55296
	ds_read_b128 v[196:199], v135 offset:56320
	s_add_i32 s29, s29, s33
	v_lshl_add_u64 v[200:201], s[16:17], 0, v[0:1]
	v_lshl_add_u64 v[200:201], v[200:201], 0, s[90:91]
	s_mov_b32 m0, s29
	v_mov_b32_e32 v0, v133
	global_load_lds_dwordx4 v[200:201], off
	s_add_i32 m0, s29, 0x2000
	s_nop 0
	v_lshl_add_u64 v[200:201], s[16:17], 0, v[0:1]
	s_add_u32 s16, s16, 0x40080
	v_lshl_add_u64 v[200:201], v[200:201], 0, s[90:91]
	s_addc_u32 s17, s17, 0
	v_mov_b32_e32 v0, v131
	s_add_i32 s29, s34, s33
	global_load_lds_dwordx4 v[200:201], off
	s_mov_b32 m0, s29
	s_nop 0
	global_load_lds_dwordx4 v0, s[16:17]
	v_mov_b32_e32 v0, v133
	s_add_i32 m0, s29, 0x2000
	s_nop 0
	global_load_lds_dwordx4 v0, s[16:17]
	s_waitcnt vmcnt(6)
	s_waitcnt lgkmcnt(0)
	s_barrier
	s_setprio 1
	s_waitcnt lgkmcnt(0)
	v_mfma_f32_16x16x32_bf16 v[94:97], v[136:139], v[168:171], v[94:97]
	v_mfma_f32_16x16x32_bf16 v[90:93], v[144:147], v[168:171], v[90:93]
	v_mfma_f32_16x16x32_bf16 v[86:89], v[136:139], v[176:179], v[86:89]
	v_mfma_f32_16x16x32_bf16 v[82:85], v[144:147], v[176:179], v[82:85]
	v_mfma_f32_16x16x32_bf16 v[78:81], v[136:139], v[184:187], v[78:81]
	v_mfma_f32_16x16x32_bf16 v[74:77], v[144:147], v[184:187], v[74:77]
	v_mfma_f32_16x16x32_bf16 v[70:73], v[136:139], v[192:195], v[70:73]
	v_mfma_f32_16x16x32_bf16 v[66:69], v[144:147], v[192:195], v[66:69]
	v_mfma_f32_16x16x32_bf16 v[94:97], v[140:143], v[172:175], v[94:97]
	v_mfma_f32_16x16x32_bf16 v[90:93], v[148:151], v[172:175], v[90:93]
	v_mfma_f32_16x16x32_bf16 v[86:89], v[140:143], v[180:183], v[86:89]
	v_mfma_f32_16x16x32_bf16 v[82:85], v[148:151], v[180:183], v[82:85]
	v_mfma_f32_16x16x32_bf16 v[78:81], v[140:143], v[188:191], v[78:81]
	v_mfma_f32_16x16x32_bf16 v[74:77], v[148:151], v[188:191], v[74:77]
	v_mfma_f32_16x16x32_bf16 v[70:73], v[140:143], v[196:199], v[70:73]
	v_mfma_f32_16x16x32_bf16 v[66:69], v[148:151], v[196:199], v[66:69]
	s_setprio 0
	s_setprio 1
	v_mfma_f32_16x16x32_bf16 v[30:33], v[152:155], v[168:171], v[30:33]
	v_mfma_f32_16x16x32_bf16 v[26:29], v[160:163], v[168:171], v[26:29]
	v_mfma_f32_16x16x32_bf16 v[22:25], v[152:155], v[176:179], v[22:25]
	v_mfma_f32_16x16x32_bf16 v[18:21], v[160:163], v[176:179], v[18:21]
	v_mfma_f32_16x16x32_bf16 v[14:17], v[152:155], v[184:187], v[14:17]
	v_mfma_f32_16x16x32_bf16 v[10:13], v[160:163], v[184:187], v[10:13]
	v_mfma_f32_16x16x32_bf16 v[6:9], v[152:155], v[192:195], v[6:9]
	v_mfma_f32_16x16x32_bf16 v[2:5], v[160:163], v[192:195], v[2:5]
	v_mfma_f32_16x16x32_bf16 v[30:33], v[156:159], v[172:175], v[30:33]
	v_mfma_f32_16x16x32_bf16 v[26:29], v[164:167], v[172:175], v[26:29]
	v_mfma_f32_16x16x32_bf16 v[22:25], v[156:159], v[180:183], v[22:25]
	v_mfma_f32_16x16x32_bf16 v[18:21], v[164:167], v[180:183], v[18:21]
	v_mfma_f32_16x16x32_bf16 v[14:17], v[156:159], v[188:191], v[14:17]
	v_mfma_f32_16x16x32_bf16 v[10:13], v[164:167], v[188:191], v[10:13]
	v_mfma_f32_16x16x32_bf16 v[6:9], v[156:159], v[196:199], v[6:9]
	v_mfma_f32_16x16x32_bf16 v[2:5], v[164:167], v[196:199], v[2:5]
	s_setprio 0
	s_barrier
	v_mov_b32_e32 v0, v130
	s_mov_b32 m0, s22
	v_lshl_add_u64 v[198:199], s[14:15], 0, v[0:1]
	v_lshl_add_u64 v[198:199], v[198:199], 0, s[90:91]
	v_mov_b32_e32 v0, v132
	global_load_lds_dwordx4 v[198:199], off
	s_mov_b32 m0, s23
	v_lshl_add_u64 v[198:199], s[14:15], 0, v[0:1]
	v_lshl_add_u64 v[198:199], v[198:199], 0, s[90:91]
	global_load_lds_dwordx4 v[198:199], off
	s_add_i32 s28, s28, 2
	s_add_u32 s12, s12, 0x100
	s_addc_u32 s13, s13, 0
	s_cmp_gt_u32 s28, 13
	s_cbranch_scc0 .LBB0_1200
	s_add_u32 s4, s6, 0x2b400000
	s_addc_u32 s5, s7, 0
	s_mul_i32 s10, s94, 0x30000
	s_mul_hi_u32 s9, s94, 0x30000
	s_add_u32 s6, s6, s10
	s_addc_u32 s7, s7, s9
	s_lshl_b32 s8, s8, 8
	s_ashr_i32 s9, s18, 5
	s_add_i32 s8, s8, s87
	s_mul_hi_i32 s10, s9, 0x6000
	s_mulk_i32 s9, 0x6000
	s_add_u32 s6, s6, s9
	v_mbcnt_lo_u32_b32 v140, -1, 0
	v_mbcnt_hi_u32_b32 v140, -1, v140
	s_addc_u32 s7, s7, s10
	s_lshl_b32 s9, s19, 8
	v_lshrrev_b32_e32 v0, 1, v140
	v_and_or_b32 v0, v0, 24, s9
	v_or_b32_e32 v200, s72, v0
	v_lshlrev_b32_e32 v0, 2, v200
	v_lshl_add_u64 v[130:131], s[6:7], 0, v[0:1]
	s_mov_b64 s[6:7], 0x102000
	v_lshl_add_u64 v[138:139], v[130:131], 0, s[6:7]
	s_mov_b32 s6, 0x102000
	v_add_co_u32_e32 v130, vcc, s6, v130
	v_and_or_b32 v174, v140, 15, s8
	s_nop 0
	v_addc_co_u32_e32 v131, vcc, 0, v131, vcc
	global_load_dwordx4 v[130:133], v[130:131], off
	s_nop 0
	global_load_dwordx4 v[134:137], v[138:139], off offset:16
	s_cmp_lg_u64 s[2:3], 0
	v_or_b32_e32 v178, 16, v174
	v_or_b32_e32 v176, 32, v174
	v_or_b32_e32 v172, 48, v174
	v_add_u32_e32 v186, 0x80, v174
	v_add_u32_e32 v184, 0x90, v174
	v_add_u32_e32 v182, 0xa0, v174
	v_add_u32_e32 v180, 0xb0, v174
	s_cselect_b64 s[6:7], -1, 0
	s_cmp_eq_u64 s[2:3], 0
	v_ashrrev_i32_e32 v175, 31, v174
	v_ashrrev_i32_e32 v179, 31, v178
	v_ashrrev_i32_e32 v177, 31, v176
	v_ashrrev_i32_e32 v173, 31, v172
	v_lshlrev_b32_e32 v170, 1, v200
	v_ashrrev_i32_e32 v187, 31, v186
	v_ashrrev_i32_e32 v185, 31, v184
	v_ashrrev_i32_e32 v183, 31, v182
	v_ashrrev_i32_e32 v181, 31, v180
	s_waitcnt vmcnt(0)
	v_pk_add_f32 v[194:195], v[132:133], 1.0 op_sel_hi:[1,0]
	v_pk_add_f32 v[192:193], v[130:131], 1.0 op_sel_hi:[1,0]
	v_pk_add_f32 v[190:191], v[136:137], 1.0 op_sel_hi:[1,0]
	v_pk_add_f32 v[188:189], v[134:135], 1.0 op_sel_hi:[1,0]
	global_load_dwordx4 v[130:133], v[138:139], off offset:528
	global_load_dwordx4 v[134:137], v[138:139], off offset:512
	s_cbranch_scc1 .LBB0_1232
	v_lshlrev_b64 v[138:139], 12, v[174:175]
	v_lshl_add_u64 v[138:139], s[2:3], 0, v[138:139]
	v_lshl_add_u64 v[142:143], v[138:139], 0, v[0:1]
	global_load_dwordx4 v[138:141], v[142:143], off offset:16
	s_nop 0
	global_load_dwordx4 v[142:145], v[142:143], off
	v_lshlrev_b64 v[146:147], 12, v[178:179]
	v_lshl_add_u64 v[146:147], s[2:3], 0, v[146:147]
	v_lshl_add_u64 v[150:151], v[146:147], 0, v[0:1]
	global_load_dwordx4 v[146:149], v[150:151], off offset:16
	s_nop 0
	global_load_dwordx4 v[150:153], v[150:151], off
	v_lshlrev_b64 v[154:155], 12, v[176:177]
	v_lshl_add_u64 v[154:155], s[2:3], 0, v[154:155]
	v_lshl_add_u64 v[158:159], v[154:155], 0, v[0:1]
	global_load_dwordx4 v[154:157], v[158:159], off offset:16
	s_nop 0
	global_load_dwordx4 v[158:161], v[158:159], off
	v_lshlrev_b64 v[162:163], 12, v[172:173]
	v_lshl_add_u64 v[162:163], s[2:3], 0, v[162:163]
	v_lshl_add_u64 v[166:167], v[162:163], 0, v[0:1]
	global_load_dwordx4 v[162:165], v[166:167], off offset:16
	s_nop 0
	global_load_dwordx4 v[166:169], v[166:167], off
	v_lshlrev_b64 v[196:197], 11, v[174:175]
	v_lshl_add_u64 v[196:197], s[4:5], 0, v[196:197]
	v_mov_b32_e32 v171, v1
	v_lshl_add_u64 v[196:197], v[196:197], 0, v[170:171]
	s_waitcnt vmcnt(7)
	v_pk_fma_f32 v[198:199], v[124:125], v[190:191], v[140:141]
	s_waitcnt vmcnt(6)
	v_pk_fma_f32 v[144:145], v[128:129], v[194:195], v[144:145]
	v_pk_fma_f32 v[142:143], v[126:127], v[192:193], v[142:143]
	v_pk_fma_f32 v[140:141], v[122:123], v[188:189], v[138:139]
	v_cvt_pk_bf16_f32 v138, v142, v143
	v_cvt_pk_bf16_f32 v139, v144, v145
	v_cvt_pk_bf16_f32 v140, v140, v141
	v_cvt_pk_bf16_f32 v141, v198, v199
	global_store_dwordx4 v[196:197], v[138:141], off
	s_waitcnt vmcnt(6)
	v_pk_fma_f32 v[144:145], v[116:117], v[190:191], v[148:149]
	v_pk_fma_f32 v[146:147], v[114:115], v[188:189], v[146:147]
	v_lshlrev_b64 v[138:139], 11, v[178:179]
	v_lshl_add_u64 v[138:139], s[4:5], 0, v[138:139]
	v_lshl_add_u64 v[142:143], v[138:139], 0, v[170:171]
	s_waitcnt vmcnt(5)
	v_pk_fma_f32 v[140:141], v[120:121], v[194:195], v[152:153]
	v_pk_fma_f32 v[138:139], v[118:119], v[192:193], v[150:151]
	v_lshlrev_b64 v[196:197], 11, v[186:187]
	v_cvt_pk_bf16_f32 v138, v138, v139
	v_cvt_pk_bf16_f32 v139, v140, v141
	v_cvt_pk_bf16_f32 v140, v146, v147
	v_cvt_pk_bf16_f32 v141, v144, v145
	global_store_dwordx4 v[142:143], v[138:141], off
	s_waitcnt vmcnt(5)
	v_pk_fma_f32 v[144:145], v[108:109], v[190:191], v[156:157]
	v_pk_fma_f32 v[146:147], v[106:107], v[188:189], v[154:155]
	v_lshlrev_b64 v[138:139], 11, v[176:177]
	v_lshl_add_u64 v[138:139], s[4:5], 0, v[138:139]
	v_lshl_add_u64 v[142:143], v[138:139], 0, v[170:171]
	s_waitcnt vmcnt(4)
	v_pk_fma_f32 v[140:141], v[112:113], v[194:195], v[160:161]
	v_pk_fma_f32 v[138:139], v[110:111], v[192:193], v[158:159]
	v_lshl_add_u64 v[196:197], s[4:5], 0, v[196:197]
	v_cvt_pk_bf16_f32 v138, v138, v139
	v_cvt_pk_bf16_f32 v139, v140, v141
	v_cvt_pk_bf16_f32 v140, v146, v147
	v_cvt_pk_bf16_f32 v141, v144, v145
	global_store_dwordx4 v[142:143], v[138:141], off
	s_waitcnt vmcnt(4)
	v_pk_fma_f32 v[144:145], v[100:101], v[190:191], v[164:165]
	v_pk_fma_f32 v[146:147], v[98:99], v[188:189], v[162:163]
	v_lshlrev_b64 v[138:139], 11, v[172:173]
	v_lshl_add_u64 v[138:139], s[4:5], 0, v[138:139]
	v_lshl_add_u64 v[142:143], v[138:139], 0, v[170:171]
	s_waitcnt vmcnt(3)
	v_pk_fma_f32 v[140:141], v[104:105], v[194:195], v[168:169]
	v_pk_fma_f32 v[138:139], v[102:103], v[192:193], v[166:167]
	v_lshl_add_u64 v[196:197], v[196:197], 0, v[170:171]
	v_cvt_pk_bf16_f32 v138, v138, v139
	v_cvt_pk_bf16_f32 v139, v140, v141
	v_cvt_pk_bf16_f32 v140, v146, v147
	v_cvt_pk_bf16_f32 v141, v144, v145
	global_store_dwordx4 v[142:143], v[138:141], off
	v_lshlrev_b64 v[146:147], 12, v[182:183]
	v_lshl_add_u64 v[146:147], s[2:3], 0, v[146:147]
	v_lshlrev_b64 v[138:139], 12, v[186:187]
	v_lshl_add_u64 v[138:139], s[2:3], 0, v[138:139]
	v_lshl_add_u64 v[138:139], v[138:139], 0, v[0:1]
	global_load_dwordx4 v[154:157], v[138:139], off offset:16
	global_load_dwordx4 v[158:161], v[138:139], off
	v_lshlrev_b64 v[138:139], 12, v[184:185]
	v_lshl_add_u64 v[138:139], s[2:3], 0, v[138:139]
	v_lshl_add_u64 v[142:143], v[138:139], 0, v[0:1]
	global_load_dwordx4 v[138:141], v[142:143], off offset:16
	s_nop 0
	global_load_dwordx4 v[142:145], v[142:143], off
	v_lshl_add_u64 v[146:147], v[146:147], 0, v[0:1]
	global_load_dwordx4 v[162:165], v[146:147], off offset:16
	global_load_dwordx4 v[166:169], v[146:147], off
	v_lshlrev_b64 v[146:147], 12, v[180:181]
	v_lshl_add_u64 v[146:147], s[2:3], 0, v[146:147]
	v_lshl_add_u64 v[150:151], v[146:147], 0, v[0:1]
	global_load_dwordx4 v[146:149], v[150:151], off offset:16
	s_nop 0
	global_load_dwordx4 v[150:153], v[150:151], off
	s_waitcnt vmcnt(7)
	v_pk_fma_f32 v[198:199], v[92:93], v[190:191], v[156:157]
	s_waitcnt vmcnt(6)
	v_pk_fma_f32 v[160:161], v[96:97], v[194:195], v[160:161]
	v_pk_fma_f32 v[158:159], v[94:95], v[192:193], v[158:159]
	v_pk_fma_f32 v[156:157], v[90:91], v[188:189], v[154:155]
	v_cvt_pk_bf16_f32 v154, v158, v159
	v_cvt_pk_bf16_f32 v155, v160, v161
	v_cvt_pk_bf16_f32 v156, v156, v157
	v_cvt_pk_bf16_f32 v157, v198, v199
	global_store_dwordx4 v[196:197], v[154:157], off
	s_waitcnt vmcnt(5)
	v_pk_fma_f32 v[144:145], v[88:89], v[194:195], v[144:145]
	v_pk_fma_f32 v[142:143], v[86:87], v[192:193], v[142:143]
	v_lshlrev_b64 v[154:155], 11, v[184:185]
	v_lshl_add_u64 v[154:155], s[4:5], 0, v[154:155]
	v_pk_fma_f32 v[156:157], v[84:85], v[190:191], v[140:141]
	v_pk_fma_f32 v[140:141], v[82:83], v[188:189], v[138:139]
	v_lshl_add_u64 v[154:155], v[154:155], 0, v[170:171]
	v_cvt_pk_bf16_f32 v138, v142, v143
	v_cvt_pk_bf16_f32 v139, v144, v145
	v_cvt_pk_bf16_f32 v140, v140, v141
	v_cvt_pk_bf16_f32 v141, v156, v157
	global_store_dwordx4 v[154:155], v[138:141], off
	s_waitcnt vmcnt(5)
	v_pk_fma_f32 v[144:145], v[76:77], v[190:191], v[164:165]
	v_pk_fma_f32 v[154:155], v[74:75], v[188:189], v[162:163]
	v_lshlrev_b64 v[138:139], 11, v[182:183]
	v_lshl_add_u64 v[138:139], s[4:5], 0, v[138:139]
	v_lshl_add_u64 v[142:143], v[138:139], 0, v[170:171]
	s_waitcnt vmcnt(4)
	v_pk_fma_f32 v[140:141], v[80:81], v[194:195], v[168:169]
	v_pk_fma_f32 v[138:139], v[78:79], v[192:193], v[166:167]
	s_waitcnt vmcnt(3)
	v_pk_fma_f32 v[146:147], v[66:67], v[188:189], v[146:147]
	v_cvt_pk_bf16_f32 v138, v138, v139
	v_cvt_pk_bf16_f32 v139, v140, v141
	v_cvt_pk_bf16_f32 v140, v154, v155
	v_cvt_pk_bf16_f32 v141, v144, v145
	global_store_dwordx4 v[142:143], v[138:141], off
	v_pk_fma_f32 v[144:145], v[68:69], v[190:191], v[148:149]
	s_nop 0
	v_lshlrev_b64 v[138:139], 11, v[180:181]
	v_lshl_add_u64 v[138:139], s[4:5], 0, v[138:139]
	v_lshl_add_u64 v[142:143], v[138:139], 0, v[170:171]
	s_waitcnt vmcnt(3)
	v_pk_fma_f32 v[140:141], v[72:73], v[194:195], v[152:153]
	v_pk_fma_f32 v[138:139], v[70:71], v[192:193], v[150:151]
	s_nop 0
	v_cvt_pk_bf16_f32 v138, v138, v139
	v_cvt_pk_bf16_f32 v139, v140, v141
	v_cvt_pk_bf16_f32 v140, v146, v147
	v_cvt_pk_bf16_f32 v141, v144, v145
	global_store_dwordx4 v[142:143], v[138:141], off
	s_cbranch_execnz .LBB0_1204

.LBB0_1612:
	s_add_u32 s36, s34, 0xfffa8080
	s_addc_u32 s37, s35, -1
	s_add_i32 s61, 0, 0x10000
	s_cmp_eq_u32 s60, 18
	s_cselect_b32 s37, s27, s37
	s_cselect_b32 s36, s26, s36
	v_add_u32_e32 v0, s61, v198
	s_cselect_b32 s39, s29, s59
	s_cselect_b32 s38, s28, s31
	s_add_i32 s64, 0, 0x14000
	ds_read_b128 v[130:133], v0
	ds_read_b128 v[134:137], v0 offset:1024
	ds_read_b128 v[138:141], v0 offset:2048
	ds_read_b128 v[142:145], v0 offset:3072
	v_add_u32_e32 v0, s64, v198
	ds_read_b128 v[146:149], v0
	ds_read_b128 v[150:153], v0 offset:1024
	ds_read_b128 v[154:157], v0 offset:2048
	ds_read_b128 v[158:161], v0 offset:3072
	v_mov_b32_e32 v0, v194
	ds_read_b128 v[162:165], v199
	ds_read_b128 v[166:169], v199 offset:1024
	ds_read_b128 v[170:173], v199 offset:2048
	ds_read_b128 v[174:177], v199 offset:3072
	ds_read_b128 v[178:181], v199 offset:4096
	ds_read_b128 v[182:185], v199 offset:5120
	ds_read_b128 v[186:189], v199 offset:6144
	ds_read_b128 v[190:193], v199 offset:7168
	s_add_i32 m0, s85, 0xc000
	s_nop 0
	global_load_lds_dwordx4 v0, s[34:35]
	v_mov_b32_e32 v0, v196
	s_add_i32 m0, s85, 0xe000
	s_nop 0
	global_load_lds_dwordx4 v0, s[34:35]
	s_waitcnt vmcnt(8)
	s_waitcnt lgkmcnt(0)
	s_barrier
	s_setprio 1
	s_waitcnt lgkmcnt(0)
	v_mfma_scale_f32_16x16x128_f8f6f4 v[126:129], v[130:137], v[162:169], v[126:129], v234, v252 op_sel_hi:[0,0,0]
	v_mfma_scale_f32_16x16x128_f8f6f4 v[122:125], v[138:145], v[162:169], v[122:125], v234, v252 op_sel_hi:[0,0,0]
	v_mfma_scale_f32_16x16x128_f8f6f4 v[118:121], v[130:137], v[170:177], v[118:121], v234, v252 op_sel_hi:[0,0,0]
	v_mfma_scale_f32_16x16x128_f8f6f4 v[114:117], v[138:145], v[170:177], v[114:117], v234, v252 op_sel_hi:[0,0,0]
	v_mfma_scale_f32_16x16x128_f8f6f4 v[110:113], v[130:137], v[178:185], v[110:113], v234, v252 op_sel_hi:[0,0,0]
	v_mfma_scale_f32_16x16x128_f8f6f4 v[106:109], v[138:145], v[178:185], v[106:109], v234, v252 op_sel_hi:[0,0,0]
	v_mfma_scale_f32_16x16x128_f8f6f4 v[102:105], v[130:137], v[186:193], v[102:105], v234, v252 op_sel_hi:[0,0,0]
	v_mfma_scale_f32_16x16x128_f8f6f4 v[98:101], v[138:145], v[186:193], v[98:101], v234, v252 op_sel_hi:[0,0,0]
	s_setprio 0
	s_setprio 1
	v_mfma_scale_f32_16x16x128_f8f6f4 v[200:203], v[146:153], v[162:169], v[62:65], v234, v252 op_sel_hi:[0,0,0]
	v_mfma_scale_f32_16x16x128_f8f6f4 v[162:165], v[154:161], v[162:169], v[58:61], v234, v252 op_sel_hi:[0,0,0]
	v_mfma_scale_f32_16x16x128_f8f6f4 v[166:169], v[146:153], v[170:177], v[54:57], v234, v252 op_sel_hi:[0,0,0]
	v_mfma_scale_f32_16x16x128_f8f6f4 v[170:173], v[154:161], v[170:177], v[50:53], v234, v252 op_sel_hi:[0,0,0]
	v_mfma_scale_f32_16x16x128_f8f6f4 v[174:177], v[146:153], v[178:185], v[46:49], v234, v252 op_sel_hi:[0,0,0]
	v_mfma_scale_f32_16x16x128_f8f6f4 v[178:181], v[154:161], v[178:185], v[42:45], v234, v252 op_sel_hi:[0,0,0]
	v_mfma_scale_f32_16x16x128_f8f6f4 v[182:185], v[146:153], v[186:193], v[38:41], v234, v252 op_sel_hi:[0,0,0]
	v_mfma_scale_f32_16x16x128_f8f6f4 v[186:189], v[154:161], v[186:193], v[34:37], v234, v252 op_sel_hi:[0,0,0]
	s_setprio 0
	s_barrier
	v_mov_b32_e32 v0, v195
	s_add_i32 s61, s61, s33
	s_nop 2
	ds_read_b128 v[34:37], v199 offset:16384
	ds_read_b128 v[38:41], v199 offset:17408
	ds_read_b128 v[42:45], v199 offset:18432
	ds_read_b128 v[46:49], v199 offset:19456
	ds_read_b128 v[50:53], v199 offset:20480
	ds_read_b128 v[54:57], v199 offset:21504
	ds_read_b128 v[58:61], v199 offset:22528
	ds_read_b128 v[62:65], v199 offset:23552
	s_mov_b32 m0, s61
	s_nop 0
	global_load_lds_dwordx4 v0, s[38:39]
	v_mov_b32_e32 v0, v197
	s_add_i32 m0, s61, 0x2000
	s_add_u32 s62, s38, 0x58000
	global_load_lds_dwordx4 v0, s[38:39]
	s_addc_u32 s63, s39, 0
	v_mov_b32_e32 v0, v195
	s_add_i32 s61, s64, s33
	s_mov_b32 m0, s61
	s_nop 0
	global_load_lds_dwordx4 v0, s[62:63]
	v_mov_b32_e32 v0, v197
	s_add_i32 m0, s61, 0x2000
	s_nop 0
	global_load_lds_dwordx4 v0, s[62:63]
	s_waitcnt vmcnt(6)
	s_waitcnt lgkmcnt(0)
	s_barrier
	s_setprio 1
	s_waitcnt lgkmcnt(0)
	v_mfma_scale_f32_16x16x128_f8f6f4 v[94:97], v[130:137], v[34:41], v[94:97], v234, v252 op_sel_hi:[0,0,0]
	v_mfma_scale_f32_16x16x128_f8f6f4 v[90:93], v[138:145], v[34:41], v[90:93], v234, v252 op_sel_hi:[0,0,0]
	v_mfma_scale_f32_16x16x128_f8f6f4 v[86:89], v[130:137], v[42:49], v[86:89], v234, v252 op_sel_hi:[0,0,0]
	v_mfma_scale_f32_16x16x128_f8f6f4 v[82:85], v[138:145], v[42:49], v[82:85], v234, v252 op_sel_hi:[0,0,0]
	v_mfma_scale_f32_16x16x128_f8f6f4 v[78:81], v[130:137], v[50:57], v[78:81], v234, v252 op_sel_hi:[0,0,0]
	v_mfma_scale_f32_16x16x128_f8f6f4 v[74:77], v[138:145], v[50:57], v[74:77], v234, v252 op_sel_hi:[0,0,0]
	v_mfma_scale_f32_16x16x128_f8f6f4 v[190:193], v[130:137], v[58:65], v[70:73], v234, v252 op_sel_hi:[0,0,0]
	v_mfma_scale_f32_16x16x128_f8f6f4 v[204:207], v[138:145], v[58:65], v[66:69], v234, v252 op_sel_hi:[0,0,0]
	s_setprio 0
	s_setprio 1
	v_mfma_scale_f32_16x16x128_f8f6f4 v[208:211], v[146:153], v[34:41], v[30:33], v234, v252 op_sel_hi:[0,0,0]
	v_mfma_scale_f32_16x16x128_f8f6f4 v[212:215], v[154:161], v[34:41], v[26:29], v234, v252 op_sel_hi:[0,0,0]
	v_mfma_scale_f32_16x16x128_f8f6f4 v[216:219], v[146:153], v[42:49], v[22:25], v234, v252 op_sel_hi:[0,0,0]
	v_mfma_scale_f32_16x16x128_f8f6f4 v[228:231], v[154:161], v[42:49], v[18:21], v234, v252 op_sel_hi:[0,0,0]
	v_mfma_scale_f32_16x16x128_f8f6f4 v[244:247], v[146:153], v[50:57], v[14:17], v234, v252 op_sel_hi:[0,0,0]
	v_mfma_scale_f32_16x16x128_f8f6f4 v[248:251], v[154:161], v[50:57], v[10:13], v234, v252 op_sel_hi:[0,0,0]
	v_mfma_scale_f32_16x16x128_f8f6f4 v[224:227], v[146:153], v[58:65], v[6:9], v234, v252 op_sel_hi:[0,0,0]
	v_mfma_scale_f32_16x16x128_f8f6f4 v[220:223], v[154:161], v[58:65], v[2:5], v234, v252 op_sel_hi:[0,0,0]
	s_setprio 0
	s_barrier
	s_add_i32 s61, 0, 0x18000
	v_add_u32_e32 v0, s61, v198
	s_add_i32 s64, 0, 0x1c000
	s_nop 1
	ds_read_b128 v[2:5], v0
	ds_read_b128 v[6:9], v0 offset:1024
	ds_read_b128 v[10:13], v0 offset:2048
	ds_read_b128 v[14:17], v0 offset:3072
	v_add_u32_e32 v0, s64, v198
	ds_read_b128 v[130:133], v0
	ds_read_b128 v[134:137], v0 offset:1024
	ds_read_b128 v[138:141], v0 offset:2048
	ds_read_b128 v[142:145], v0 offset:3072
	s_add_u32 s62, s36, 0x58000
	ds_read_b128 v[18:21], v199 offset:32768
	ds_read_b128 v[22:25], v199 offset:33792
	ds_read_b128 v[26:29], v199 offset:34816
	ds_read_b128 v[30:33], v199 offset:35840
	ds_read_b128 v[34:37], v199 offset:36864
	ds_read_b128 v[38:41], v199 offset:37888
	ds_read_b128 v[66:69], v199 offset:38912
	ds_read_b128 v[70:73], v199 offset:39936
	s_addc_u32 s63, s37, 0
	v_mov_b32_e32 v0, v194
	s_mov_b32 m0, s85
	s_nop 0
	global_load_lds_dwordx4 v0, s[36:37]
	v_mov_b32_e32 v0, v196
	s_mov_b32 m0, s3
	s_nop 0
	global_load_lds_dwordx4 v0, s[36:37]
	v_mov_b32_e32 v0, v194
	s_mov_b32 m0, s45
	s_nop 0
	global_load_lds_dwordx4 v0, s[62:63]
	v_mov_b32_e32 v0, v196
	s_mov_b32 m0, s47
	s_nop 0
	global_load_lds_dwordx4 v0, s[62:63]
	s_waitcnt vmcnt(8)
	s_waitcnt lgkmcnt(0)
	s_barrier
	s_setprio 1
	s_waitcnt lgkmcnt(0)
	v_mfma_scale_f32_16x16x128_f8f6f4 v[126:129], v[2:9], v[18:25], v[126:129], v234, v252 op_sel_hi:[0,0,0]
	v_mfma_scale_f32_16x16x128_f8f6f4 v[122:125], v[10:17], v[18:25], v[122:125], v234, v252 op_sel_hi:[0,0,0]
	v_mfma_scale_f32_16x16x128_f8f6f4 v[118:121], v[2:9], v[26:33], v[118:121], v234, v252 op_sel_hi:[0,0,0]
	v_mfma_scale_f32_16x16x128_f8f6f4 v[114:117], v[10:17], v[26:33], v[114:117], v234, v252 op_sel_hi:[0,0,0]
	v_mfma_scale_f32_16x16x128_f8f6f4 v[110:113], v[2:9], v[34:41], v[110:113], v234, v252 op_sel_hi:[0,0,0]
	v_mfma_scale_f32_16x16x128_f8f6f4 v[106:109], v[10:17], v[34:41], v[106:109], v234, v252 op_sel_hi:[0,0,0]
	v_mfma_scale_f32_16x16x128_f8f6f4 v[102:105], v[2:9], v[66:73], v[102:105], v234, v252 op_sel_hi:[0,0,0]
	v_mfma_scale_f32_16x16x128_f8f6f4 v[98:101], v[10:17], v[66:73], v[98:101], v234, v252 op_sel_hi:[0,0,0]
	s_setprio 0
	s_setprio 1
	v_mfma_scale_f32_16x16x128_f8f6f4 v[62:65], v[130:137], v[18:25], v[200:203], v234, v252 op_sel_hi:[0,0,0]
	v_mfma_scale_f32_16x16x128_f8f6f4 v[58:61], v[138:145], v[18:25], v[162:165], v234, v252 op_sel_hi:[0,0,0]
	v_mfma_scale_f32_16x16x128_f8f6f4 v[54:57], v[130:137], v[26:33], v[166:169], v234, v252 op_sel_hi:[0,0,0]
	v_mfma_scale_f32_16x16x128_f8f6f4 v[50:53], v[138:145], v[26:33], v[170:173], v234, v252 op_sel_hi:[0,0,0]
	v_mfma_scale_f32_16x16x128_f8f6f4 v[46:49], v[130:137], v[34:41], v[174:177], v234, v252 op_sel_hi:[0,0,0]
	v_mfma_scale_f32_16x16x128_f8f6f4 v[42:45], v[138:145], v[34:41], v[178:181], v234, v252 op_sel_hi:[0,0,0]
	v_mfma_scale_f32_16x16x128_f8f6f4 v[38:41], v[130:137], v[66:73], v[182:185], v234, v252 op_sel_hi:[0,0,0]
	v_mfma_scale_f32_16x16x128_f8f6f4 v[34:37], v[138:145], v[66:73], v[186:189], v234, v252 op_sel_hi:[0,0,0]
	s_setprio 0
	s_barrier
	v_mov_b32_e32 v0, v195
	ds_read_b128 v[18:21], v199 offset:49152
	ds_read_b128 v[22:25], v199 offset:50176
	ds_read_b128 v[146:149], v199 offset:51200
	ds_read_b128 v[150:153], v199 offset:52224
	ds_read_b128 v[154:157], v199 offset:53248
	ds_read_b128 v[158:161], v199 offset:54272
	ds_read_b128 v[162:165], v199 offset:55296
	ds_read_b128 v[166:169], v199 offset:56320
	s_add_i32 s61, s61, s33
	v_lshl_add_u64 v[26:27], s[38:39], 0, v[0:1]
	v_lshl_add_u64 v[26:27], v[26:27], 0, s[90:91]
	s_mov_b32 m0, s61
	v_mov_b32_e32 v0, v197
	global_load_lds_dwordx4 v[26:27], off
	s_add_i32 m0, s61, 0x2000
	s_nop 0
	v_lshl_add_u64 v[26:27], s[38:39], 0, v[0:1]
	s_add_u32 s38, s38, 0x58080
	v_lshl_add_u64 v[26:27], v[26:27], 0, s[90:91]
	s_addc_u32 s39, s39, 0
	v_mov_b32_e32 v0, v195
	s_add_i32 s61, s64, s33
	global_load_lds_dwordx4 v[26:27], off
	s_mov_b32 m0, s61
	s_nop 0
	global_load_lds_dwordx4 v0, s[38:39]
	v_mov_b32_e32 v0, v197
	s_add_i32 m0, s61, 0x2000
	s_nop 0
	global_load_lds_dwordx4 v0, s[38:39]
	s_waitcnt vmcnt(6)
	s_waitcnt lgkmcnt(0)
	s_barrier
	s_setprio 1
	s_waitcnt lgkmcnt(0)
	v_mfma_scale_f32_16x16x128_f8f6f4 v[94:97], v[2:9], v[18:25], v[94:97], v234, v252 op_sel_hi:[0,0,0]
	v_mfma_scale_f32_16x16x128_f8f6f4 v[90:93], v[10:17], v[18:25], v[90:93], v234, v252 op_sel_hi:[0,0,0]
	v_mfma_scale_f32_16x16x128_f8f6f4 v[86:89], v[2:9], v[146:153], v[86:89], v234, v252 op_sel_hi:[0,0,0]
	v_mfma_scale_f32_16x16x128_f8f6f4 v[82:85], v[10:17], v[146:153], v[82:85], v234, v252 op_sel_hi:[0,0,0]
	v_mfma_scale_f32_16x16x128_f8f6f4 v[78:81], v[2:9], v[154:161], v[78:81], v234, v252 op_sel_hi:[0,0,0]
	v_mfma_scale_f32_16x16x128_f8f6f4 v[74:77], v[10:17], v[154:161], v[74:77], v234, v252 op_sel_hi:[0,0,0]
	v_mfma_scale_f32_16x16x128_f8f6f4 v[70:73], v[2:9], v[162:169], v[190:193], v234, v252 op_sel_hi:[0,0,0]
	v_mfma_scale_f32_16x16x128_f8f6f4 v[66:69], v[10:17], v[162:169], v[204:207], v234, v252 op_sel_hi:[0,0,0]
	s_setprio 0
	s_setprio 1
	v_mfma_scale_f32_16x16x128_f8f6f4 v[30:33], v[130:137], v[18:25], v[208:211], v234, v252 op_sel_hi:[0,0,0]
	v_mfma_scale_f32_16x16x128_f8f6f4 v[26:29], v[138:145], v[18:25], v[212:215], v234, v252 op_sel_hi:[0,0,0]
	v_mfma_scale_f32_16x16x128_f8f6f4 v[22:25], v[130:137], v[146:153], v[216:219], v234, v252 op_sel_hi:[0,0,0]
	v_mfma_scale_f32_16x16x128_f8f6f4 v[18:21], v[138:145], v[146:153], v[228:231], v234, v252 op_sel_hi:[0,0,0]
	v_mfma_scale_f32_16x16x128_f8f6f4 v[14:17], v[130:137], v[154:161], v[244:247], v234, v252 op_sel_hi:[0,0,0]
	v_mfma_scale_f32_16x16x128_f8f6f4 v[10:13], v[138:145], v[154:161], v[248:251], v234, v252 op_sel_hi:[0,0,0]
	v_mfma_scale_f32_16x16x128_f8f6f4 v[6:9], v[130:137], v[162:169], v[224:227], v234, v252 op_sel_hi:[0,0,0]
	v_mfma_scale_f32_16x16x128_f8f6f4 v[2:5], v[138:145], v[162:169], v[220:223], v234, v252 op_sel_hi:[0,0,0]
	s_setprio 0
	s_barrier
	v_mov_b32_e32 v0, v194
	s_mov_b32 m0, s50
	v_lshl_add_u64 v[190:191], s[36:37], 0, v[0:1]
	v_lshl_add_u64 v[190:191], v[190:191], 0, s[90:91]
	v_mov_b32_e32 v0, v196
	global_load_lds_dwordx4 v[190:191], off
	s_mov_b32 m0, s51
	v_lshl_add_u64 v[190:191], s[36:37], 0, v[0:1]
	v_lshl_add_u64 v[190:191], v[190:191], 0, s[90:91]
	global_load_lds_dwordx4 v[190:191], off
	s_add_i32 s60, s60, 2
	s_add_u32 s34, s34, 0x100
	s_addc_u32 s35, s35, 0
	s_add_u32 s31, s31, 0x100
	s_addc_u32 s59, s59, 0
	s_cmp_gt_u32 s60, 19
	s_cbranch_scc0 .LBB0_1612
	v_readlane_b32 s34, v254, 19
	v_readlane_b32 s35, v254, 20
	s_and_b64 vcc, exec, s[34:35]
	s_cbranch_vccz .LBB0_1615
	s_barrier

.LBB0_1670:
	s_add_u32 s36, s34, 0xfffa8080
	s_addc_u32 s37, s35, -1
	s_add_i32 s60, 0, 0x10000
	s_cmp_eq_u32 s59, 18
	s_cselect_b32 s37, s27, s37
	s_cselect_b32 s36, s26, s36
	v_add_u32_e32 v0, s60, v143
	s_cselect_b32 s39, s29, s58
	s_cselect_b32 s38, s28, s31
	s_add_i32 s62, 0, 0x14000
	ds_read_b128 v[146:149], v0
	ds_read_b128 v[150:153], v0 offset:1024
	ds_read_b128 v[154:157], v0 offset:2048
	ds_read_b128 v[158:161], v0 offset:3072
	v_add_u32_e32 v0, s62, v143
	ds_read_b128 v[162:165], v0
	ds_read_b128 v[166:169], v0 offset:1024
	ds_read_b128 v[170:173], v0 offset:2048
	ds_read_b128 v[174:177], v0 offset:3072
	v_mov_b32_e32 v0, v253
	ds_read_b128 v[178:181], v145
	ds_read_b128 v[182:185], v145 offset:1024
	ds_read_b128 v[186:189], v145 offset:2048
	ds_read_b128 v[190:193], v145 offset:3072
	ds_read_b128 v[194:197], v145 offset:4096
	ds_read_b128 v[198:201], v145 offset:5120
	ds_read_b128 v[202:205], v145 offset:6144
	ds_read_b128 v[206:209], v145 offset:7168
	s_add_i32 m0, s85, 0xc000
	s_nop 0
	global_load_lds_dwordx4 v0, s[34:35]
	v_mov_b32_e32 v0, v242
	s_add_i32 m0, s85, 0xe000
	s_nop 0
	global_load_lds_dwordx4 v0, s[34:35]
	s_waitcnt vmcnt(8)
	s_waitcnt lgkmcnt(0)
	s_barrier
	s_setprio 1
	s_waitcnt lgkmcnt(0)
	v_mfma_scale_f32_16x16x128_f8f6f4 v[126:129], v[146:153], v[178:185], v[126:129], v234, v252 op_sel_hi:[0,0,0]
	v_mfma_scale_f32_16x16x128_f8f6f4 v[122:125], v[154:161], v[178:185], v[122:125], v234, v252 op_sel_hi:[0,0,0]
	v_mfma_scale_f32_16x16x128_f8f6f4 v[110:113], v[146:153], v[186:193], v[110:113], v234, v252 op_sel_hi:[0,0,0]
	v_mfma_scale_f32_16x16x128_f8f6f4 v[106:109], v[154:161], v[186:193], v[106:109], v234, v252 op_sel_hi:[0,0,0]
	v_mfma_scale_f32_16x16x128_f8f6f4 v[210:213], v[146:153], v[194:201], v[94:97], v234, v252 op_sel_hi:[0,0,0]
	v_mfma_scale_f32_16x16x128_f8f6f4 v[214:217], v[154:161], v[194:201], v[90:93], v234, v252 op_sel_hi:[0,0,0]
	v_mfma_scale_f32_16x16x128_f8f6f4 v[218:221], v[146:153], v[202:209], v[78:81], v234, v252 op_sel_hi:[0,0,0]
	v_mfma_scale_f32_16x16x128_f8f6f4 v[222:225], v[154:161], v[202:209], v[74:77], v234, v252 op_sel_hi:[0,0,0]
	s_setprio 0
	s_setprio 1
	v_mfma_scale_f32_16x16x128_f8f6f4 v[118:121], v[162:169], v[178:185], v[118:121], v234, v252 op_sel_hi:[0,0,0]
	v_mfma_scale_f32_16x16x128_f8f6f4 v[114:117], v[170:177], v[178:185], v[114:117], v234, v252 op_sel_hi:[0,0,0]
	v_mfma_scale_f32_16x16x128_f8f6f4 v[102:105], v[162:169], v[186:193], v[102:105], v234, v252 op_sel_hi:[0,0,0]
	v_mfma_scale_f32_16x16x128_f8f6f4 v[98:101], v[170:177], v[186:193], v[98:101], v234, v252 op_sel_hi:[0,0,0]
	v_mfma_scale_f32_16x16x128_f8f6f4 v[178:181], v[162:169], v[194:201], v[86:89], v234, v252 op_sel_hi:[0,0,0]
	v_mfma_scale_f32_16x16x128_f8f6f4 v[182:185], v[170:177], v[194:201], v[82:85], v234, v252 op_sel_hi:[0,0,0]
	v_mfma_scale_f32_16x16x128_f8f6f4 v[186:189], v[162:169], v[202:209], v[70:73], v234, v252 op_sel_hi:[0,0,0]
	v_mfma_scale_f32_16x16x128_f8f6f4 v[190:193], v[170:177], v[202:209], v[66:69], v234, v252 op_sel_hi:[0,0,0]
	s_setprio 0
	s_barrier
	v_mov_b32_e32 v0, v243
	s_add_i32 s60, s60, s33
	s_nop 2
	ds_read_b128 v[66:69], v145 offset:16384
	ds_read_b128 v[70:73], v145 offset:17408
	ds_read_b128 v[74:77], v145 offset:18432
	ds_read_b128 v[78:81], v145 offset:19456
	ds_read_b128 v[82:85], v145 offset:20480
	ds_read_b128 v[86:89], v145 offset:21504
	ds_read_b128 v[90:93], v145 offset:22528
	ds_read_b128 v[94:97], v145 offset:23552
	s_mov_b32 m0, s60
	s_nop 0
	global_load_lds_dwordx4 v0, s[38:39]
	v_mov_b32_e32 v0, v142
	s_add_i32 m0, s60, 0x2000
	s_add_u32 s60, s38, 0x58000
	global_load_lds_dwordx4 v0, s[38:39]
	s_addc_u32 s61, s39, 0
	v_mov_b32_e32 v0, v243
	s_add_i32 s62, s62, s33
	s_mov_b32 m0, s62
	s_nop 0
	global_load_lds_dwordx4 v0, s[60:61]
	v_mov_b32_e32 v0, v142
	s_add_i32 m0, s62, 0x2000
	s_nop 0
	global_load_lds_dwordx4 v0, s[60:61]
	s_waitcnt vmcnt(6)
	s_waitcnt lgkmcnt(0)
	s_barrier
	s_setprio 1
	s_waitcnt lgkmcnt(0)
	v_mfma_scale_f32_16x16x128_f8f6f4 v[62:65], v[146:153], v[66:73], v[62:65], v234, v252 op_sel_hi:[0,0,0]
	v_mfma_scale_f32_16x16x128_f8f6f4 v[58:61], v[154:161], v[66:73], v[58:61], v234, v252 op_sel_hi:[0,0,0]
	v_mfma_scale_f32_16x16x128_f8f6f4 v[54:57], v[146:153], v[74:81], v[54:57], v234, v252 op_sel_hi:[0,0,0]
	v_mfma_scale_f32_16x16x128_f8f6f4 v[194:197], v[154:161], v[74:81], v[46:49], v234, v252 op_sel_hi:[0,0,0]
	v_mfma_scale_f32_16x16x128_f8f6f4 v[198:201], v[146:153], v[82:89], v[38:41], v234, v252 op_sel_hi:[0,0,0]
	v_mfma_scale_f32_16x16x128_f8f6f4 v[202:205], v[154:161], v[82:89], v[30:33], v234, v252 op_sel_hi:[0,0,0]
	v_mfma_scale_f32_16x16x128_f8f6f4 v[206:209], v[146:153], v[90:97], v[22:25], v234, v252 op_sel_hi:[0,0,0]
	v_mfma_scale_f32_16x16x128_f8f6f4 v[226:229], v[154:161], v[90:97], v[14:17], v234, v252 op_sel_hi:[0,0,0]
	s_setprio 0
	s_setprio 1
	v_mfma_scale_f32_16x16x128_f8f6f4 v[50:53], v[162:169], v[66:73], v[50:53], v234, v252 op_sel_hi:[0,0,0]
	v_mfma_scale_f32_16x16x128_f8f6f4 v[244:247], v[170:177], v[66:73], v[42:45], v234, v252 op_sel_hi:[0,0,0]
	v_mfma_scale_f32_16x16x128_f8f6f4 v[248:251], v[162:169], v[74:81], v[34:37], v234, v252 op_sel_hi:[0,0,0]
	v_mfma_scale_f32_16x16x128_f8f6f4 v[236:239], v[170:177], v[74:81], v[26:29], v234, v252 op_sel_hi:[0,0,0]
	v_mfma_scale_f32_16x16x128_f8f6f4 v[230:233], v[162:169], v[82:89], v[18:21], v234, v252 op_sel_hi:[0,0,0]
	v_mfma_scale_f32_16x16x128_f8f6f4 v[130:133], v[170:177], v[82:89], v[10:13], v234, v252 op_sel_hi:[0,0,0]
	v_mfma_scale_f32_16x16x128_f8f6f4 v[134:137], v[162:169], v[90:97], v[6:9], v234, v252 op_sel_hi:[0,0,0]
	v_mfma_scale_f32_16x16x128_f8f6f4 v[138:141], v[170:177], v[90:97], v[2:5], v234, v252 op_sel_hi:[0,0,0]
	s_setprio 0
	s_barrier
	s_add_i32 s62, 0, 0x18000
	v_add_u32_e32 v0, s62, v143
	s_add_i32 s63, 0, 0x1c000
	s_nop 1
	ds_read_b128 v[2:5], v0
	ds_read_b128 v[6:9], v0 offset:1024
	ds_read_b128 v[10:13], v0 offset:2048
	ds_read_b128 v[14:17], v0 offset:3072
	v_add_u32_e32 v0, s63, v143
	ds_read_b128 v[146:149], v0
	ds_read_b128 v[150:153], v0 offset:1024
	ds_read_b128 v[154:157], v0 offset:2048
	ds_read_b128 v[158:161], v0 offset:3072
	s_add_u32 s60, s36, 0x58000
	ds_read_b128 v[18:21], v145 offset:32768
	ds_read_b128 v[22:25], v145 offset:33792
	ds_read_b128 v[26:29], v145 offset:34816
	ds_read_b128 v[30:33], v145 offset:35840
	ds_read_b128 v[34:37], v145 offset:36864
	ds_read_b128 v[38:41], v145 offset:37888
	ds_read_b128 v[42:45], v145 offset:38912
	ds_read_b128 v[46:49], v145 offset:39936
	s_addc_u32 s61, s37, 0
	v_mov_b32_e32 v0, v253
	s_mov_b32 m0, s85
	s_nop 0
	global_load_lds_dwordx4 v0, s[36:37]
	v_mov_b32_e32 v0, v242
	s_mov_b32 m0, s50
	s_nop 0
	global_load_lds_dwordx4 v0, s[36:37]
	v_mov_b32_e32 v0, v253
	s_mov_b32 m0, s51
	s_nop 0
	global_load_lds_dwordx4 v0, s[60:61]
	v_mov_b32_e32 v0, v242
	s_mov_b32 m0, s52
	s_nop 0
	global_load_lds_dwordx4 v0, s[60:61]
	s_waitcnt vmcnt(8)
	s_waitcnt lgkmcnt(0)
	s_barrier
	s_setprio 1
	s_waitcnt lgkmcnt(0)
	v_mfma_scale_f32_16x16x128_f8f6f4 v[126:129], v[2:9], v[18:25], v[126:129], v234, v252 op_sel_hi:[0,0,0]
	v_mfma_scale_f32_16x16x128_f8f6f4 v[122:125], v[10:17], v[18:25], v[122:125], v234, v252 op_sel_hi:[0,0,0]
	v_mfma_scale_f32_16x16x128_f8f6f4 v[110:113], v[2:9], v[26:33], v[110:113], v234, v252 op_sel_hi:[0,0,0]
	v_mfma_scale_f32_16x16x128_f8f6f4 v[106:109], v[10:17], v[26:33], v[106:109], v234, v252 op_sel_hi:[0,0,0]
	v_mfma_scale_f32_16x16x128_f8f6f4 v[94:97], v[2:9], v[34:41], v[210:213], v234, v252 op_sel_hi:[0,0,0]
	v_mfma_scale_f32_16x16x128_f8f6f4 v[90:93], v[10:17], v[34:41], v[214:217], v234, v252 op_sel_hi:[0,0,0]
	v_mfma_scale_f32_16x16x128_f8f6f4 v[78:81], v[2:9], v[42:49], v[218:221], v234, v252 op_sel_hi:[0,0,0]
	v_mfma_scale_f32_16x16x128_f8f6f4 v[74:77], v[10:17], v[42:49], v[222:225], v234, v252 op_sel_hi:[0,0,0]
	s_setprio 0
	s_setprio 1
	v_mfma_scale_f32_16x16x128_f8f6f4 v[118:121], v[146:153], v[18:25], v[118:121], v234, v252 op_sel_hi:[0,0,0]
	v_mfma_scale_f32_16x16x128_f8f6f4 v[114:117], v[154:161], v[18:25], v[114:117], v234, v252 op_sel_hi:[0,0,0]
	v_mfma_scale_f32_16x16x128_f8f6f4 v[102:105], v[146:153], v[26:33], v[102:105], v234, v252 op_sel_hi:[0,0,0]
	v_mfma_scale_f32_16x16x128_f8f6f4 v[98:101], v[154:161], v[26:33], v[98:101], v234, v252 op_sel_hi:[0,0,0]
	v_mfma_scale_f32_16x16x128_f8f6f4 v[86:89], v[146:153], v[34:41], v[178:181], v234, v252 op_sel_hi:[0,0,0]
	v_mfma_scale_f32_16x16x128_f8f6f4 v[82:85], v[154:161], v[34:41], v[182:185], v234, v252 op_sel_hi:[0,0,0]
	v_mfma_scale_f32_16x16x128_f8f6f4 v[70:73], v[146:153], v[42:49], v[186:189], v234, v252 op_sel_hi:[0,0,0]
	v_mfma_scale_f32_16x16x128_f8f6f4 v[66:69], v[154:161], v[42:49], v[190:193], v234, v252 op_sel_hi:[0,0,0]
	s_setprio 0
	s_barrier
	v_mov_b32_e32 v0, v243
	ds_read_b128 v[162:165], v145 offset:49152
	ds_read_b128 v[166:169], v145 offset:50176
	ds_read_b128 v[170:173], v145 offset:51200
	ds_read_b128 v[174:177], v145 offset:52224
	ds_read_b128 v[178:181], v145 offset:53248
	ds_read_b128 v[182:185], v145 offset:54272
	ds_read_b128 v[186:189], v145 offset:55296
	ds_read_b128 v[190:193], v145 offset:56320
	s_add_i32 s60, s62, s33
	v_lshl_add_u64 v[18:19], s[38:39], 0, v[0:1]
	v_lshl_add_u64 v[18:19], v[18:19], 0, s[90:91]
	s_mov_b32 m0, s60
	v_mov_b32_e32 v0, v142
	global_load_lds_dwordx4 v[18:19], off
	s_add_i32 m0, s60, 0x2000
	s_nop 0
	v_lshl_add_u64 v[18:19], s[38:39], 0, v[0:1]
	s_add_u32 s38, s38, 0x58080
	v_lshl_add_u64 v[18:19], v[18:19], 0, s[90:91]
	s_addc_u32 s39, s39, 0
	v_mov_b32_e32 v0, v243
	s_add_i32 s60, s63, s33
	global_load_lds_dwordx4 v[18:19], off
	s_mov_b32 m0, s60
	s_nop 0
	global_load_lds_dwordx4 v0, s[38:39]
	v_mov_b32_e32 v0, v142
	s_add_i32 m0, s60, 0x2000
	s_nop 0
	global_load_lds_dwordx4 v0, s[38:39]
	s_waitcnt vmcnt(6)
	s_waitcnt lgkmcnt(0)
	s_barrier
	s_setprio 1
	s_waitcnt lgkmcnt(0)
	v_mfma_scale_f32_16x16x128_f8f6f4 v[62:65], v[2:9], v[162:169], v[62:65], v234, v252 op_sel_hi:[0,0,0]
	v_mfma_scale_f32_16x16x128_f8f6f4 v[58:61], v[10:17], v[162:169], v[58:61], v234, v252 op_sel_hi:[0,0,0]
	v_mfma_scale_f32_16x16x128_f8f6f4 v[54:57], v[2:9], v[170:177], v[54:57], v234, v252 op_sel_hi:[0,0,0]
	v_mfma_scale_f32_16x16x128_f8f6f4 v[46:49], v[10:17], v[170:177], v[194:197], v234, v252 op_sel_hi:[0,0,0]
	v_mfma_scale_f32_16x16x128_f8f6f4 v[38:41], v[2:9], v[178:185], v[198:201], v234, v252 op_sel_hi:[0,0,0]
	v_mfma_scale_f32_16x16x128_f8f6f4 v[30:33], v[10:17], v[178:185], v[202:205], v234, v252 op_sel_hi:[0,0,0]
	v_mfma_scale_f32_16x16x128_f8f6f4 v[22:25], v[2:9], v[186:193], v[206:209], v234, v252 op_sel_hi:[0,0,0]
	v_mfma_scale_f32_16x16x128_f8f6f4 v[14:17], v[10:17], v[186:193], v[226:229], v234, v252 op_sel_hi:[0,0,0]
	s_setprio 0
	s_setprio 1
	v_mfma_scale_f32_16x16x128_f8f6f4 v[50:53], v[146:153], v[162:169], v[50:53], v234, v252 op_sel_hi:[0,0,0]
	v_mfma_scale_f32_16x16x128_f8f6f4 v[42:45], v[154:161], v[162:169], v[244:247], v234, v252 op_sel_hi:[0,0,0]
	v_mfma_scale_f32_16x16x128_f8f6f4 v[34:37], v[146:153], v[170:177], v[248:251], v234, v252 op_sel_hi:[0,0,0]
	v_mfma_scale_f32_16x16x128_f8f6f4 v[26:29], v[154:161], v[170:177], v[236:239], v234, v252 op_sel_hi:[0,0,0]
	v_mfma_scale_f32_16x16x128_f8f6f4 v[18:21], v[146:153], v[178:185], v[230:233], v234, v252 op_sel_hi:[0,0,0]
	v_mfma_scale_f32_16x16x128_f8f6f4 v[10:13], v[154:161], v[178:185], v[130:133], v234, v252 op_sel_hi:[0,0,0]
	v_mfma_scale_f32_16x16x128_f8f6f4 v[6:9], v[146:153], v[186:193], v[134:137], v234, v252 op_sel_hi:[0,0,0]
	v_mfma_scale_f32_16x16x128_f8f6f4 v[2:5], v[154:161], v[186:193], v[138:141], v234, v252 op_sel_hi:[0,0,0]
	s_setprio 0
	s_barrier
	v_mov_b32_e32 v0, v253
	s_mov_b32 m0, s53
	v_lshl_add_u64 v[198:199], s[36:37], 0, v[0:1]
	v_lshl_add_u64 v[198:199], v[198:199], 0, s[90:91]
	v_mov_b32_e32 v0, v242
	global_load_lds_dwordx4 v[198:199], off
	s_mov_b32 m0, s54
	v_lshl_add_u64 v[198:199], s[36:37], 0, v[0:1]
	v_lshl_add_u64 v[198:199], v[198:199], 0, s[90:91]
	global_load_lds_dwordx4 v[198:199], off
	s_add_i32 s59, s59, 2
	s_add_u32 s34, s34, 0x100
	s_addc_u32 s35, s35, 0
	s_add_u32 s31, s31, 0x100
	s_addc_u32 s58, s58, 0
	s_cmp_gt_u32 s59, 19
	s_cbranch_scc0 .LBB0_1670
	v_readlane_b32 s34, v254, 19
	v_readlane_b32 s35, v254, 20
	s_and_b64 vcc, exec, s[34:35]
	s_cbranch_vccz .LBB0_1673
	s_barrier
